# v6: hand-scheduled RWKV scan consumer + GLA-scan conversion tiles moved to WGs freed from in0/in1 GEMM rounds + flat->global nt conversion traffic + counted vmcnt in GLA loop
# baseline (speedup 1.0000x reference)
.LBB0_627:
	s_setprio 3
	s_sub_i32 s56, s2, 32
	s_add_i32 s57, s2, 0xfffffee0
	s_cmp_lt_u32 s79, 8
	s_cselect_b32 s56, s56, s57
	s_cselect_b32 s57, s81, 0x1000
	s_cselect_b32 s58, s3, s78
	ds_read_b128 v[94:97], v197 offset:16
	ds_read_b128 v[102:105], v197 offset:48
	ds_read_b32 v204, v198 offset:1280
	ds_read_b128 v[98:101], v197 offset:32
	ds_read_b128 v[90:93], v197
	ds_read_b128 v[106:109], v197 offset:64
	ds_read_b128 v[114:117], v197 offset:1360
	ds_read_b128 v[122:125], v197 offset:1392
	ds_read_b32 v206, v198 offset:2624
	ds_read_b128 v[118:121], v197 offset:1376
	ds_read_b128 v[110:113], v197 offset:1344
	ds_read_b128 v[126:129], v197 offset:1408
	s_waitcnt lgkmcnt(6)
	v_pk_mul_f32 v[210:211], v[156:157], v[94:95]
	s_nop 0
	v_pk_fma_f32 v[210:211], v[158:159], v[96:97], v[210:211]
	s_nop 0
	v_add_f32_e32 v210, v210, v211
	s_nop 0
	v_pk_mul_f32 v[214:215], v[102:103], v[204:205] op_sel_hi:[1,0]
	v_add_f32_dpp v210, v210, v210 quad_perm:[1,0,3,2] row_mask:0xf bank_mask:0xf bound_ctrl:1
	s_nop 0
	v_pk_mul_f32 v[216:217], v[104:105], v[204:205] op_sel_hi:[1,0]
	v_add_f32_dpp v210, v210, v210 quad_perm:[2,3,0,1] row_mask:0xf bank_mask:0xf bound_ctrl:1
	s_nop 0
	ds_read_b128 v[224:227], v197 offset:2704
	v_add_f32_dpp v210, v210, v210 row_half_mirror row_mask:0xf bank_mask:0xf bound_ctrl:1
	s_nop 0
	ds_read_b128 v[232:235], v197 offset:2736
	v_add_f32_dpp v218, v210, v210 row_mirror row_mask:0xf bank_mask:0xf bound_ctrl:1
	s_nop 0
	ds_read_b32 v208, v198 offset:3968
	v_pk_fma_f32 v[214:215], v[218:219], v[98:99], v[214:215] op_sel_hi:[0,1,1]
	v_pk_fma_f32 v[216:217], v[218:219], v[100:101], v[216:217] op_sel_hi:[0,1,1]
	s_nop 0
	v_pk_fma_f32 v[156:157], v[156:157], v[90:91], v[214:215]
	v_pk_fma_f32 v[158:159], v[158:159], v[92:93], v[216:217]
	ds_read_b128 v[228:231], v197 offset:2720
	ds_read_b128 v[220:223], v197 offset:2688
	ds_read_b128 v[236:239], v197 offset:2752
	s_waitcnt lgkmcnt(6)
	v_pk_mul_f32 v[210:211], v[156:157], v[114:115]
	v_pk_mul_f32 v[212:213], v[106:107], v[156:157]
	v_pk_fma_f32 v[210:211], v[158:159], v[116:117], v[210:211]
	v_pk_fma_f32 v[212:213], v[158:159], v[108:109], v[212:213]
	v_add_f32_e32 v210, v210, v211
	v_add_f32_e32 v212, v212, v213
	v_pk_mul_f32 v[214:215], v[122:123], v[206:207] op_sel_hi:[1,0]
	v_add_f32_dpp v210, v210, v210 quad_perm:[1,0,3,2] row_mask:0xf bank_mask:0xf bound_ctrl:1
	v_add_f32_dpp v212, v212, v212 quad_perm:[1,0,3,2] row_mask:0xf bank_mask:0xf bound_ctrl:1
	v_pk_mul_f32 v[216:217], v[124:125], v[206:207] op_sel_hi:[1,0]
	v_add_f32_dpp v210, v210, v210 quad_perm:[2,3,0,1] row_mask:0xf bank_mask:0xf bound_ctrl:1
	v_add_f32_dpp v212, v212, v212 quad_perm:[2,3,0,1] row_mask:0xf bank_mask:0xf bound_ctrl:1
	ds_read_b128 v[94:97], v197 offset:4048
	v_add_f32_dpp v210, v210, v210 row_half_mirror row_mask:0xf bank_mask:0xf bound_ctrl:1
	v_add_f32_dpp v212, v212, v212 row_half_mirror row_mask:0xf bank_mask:0xf bound_ctrl:1
	ds_read_b128 v[102:105], v197 offset:4080
	v_add_f32_dpp v218, v210, v210 row_mirror row_mask:0xf bank_mask:0xf bound_ctrl:1
	v_add_f32_dpp v240, v212, v212 row_mirror row_mask:0xf bank_mask:0xf bound_ctrl:1
	ds_read_b32 v204, v198 offset:5312
	v_pk_fma_f32 v[214:215], v[218:219], v[118:119], v[214:215] op_sel_hi:[0,1,1]
	v_pk_fma_f32 v[216:217], v[218:219], v[120:121], v[216:217] op_sel_hi:[0,1,1]
	v_cndmask_b32_e64 v241, 0, v240, s[4:5]
	v_pk_fma_f32 v[156:157], v[156:157], v[110:111], v[214:215]
	v_pk_fma_f32 v[158:159], v[158:159], v[112:113], v[216:217]
	ds_read_b128 v[98:101], v197 offset:4064
	ds_read_b128 v[90:93], v197 offset:4032
	ds_read_b128 v[106:109], v197 offset:4096
	s_waitcnt lgkmcnt(6)
	v_pk_mul_f32 v[210:211], v[156:157], v[224:225]
	v_pk_mul_f32 v[212:213], v[126:127], v[156:157]
	v_pk_fma_f32 v[210:211], v[158:159], v[226:227], v[210:211]
	v_pk_fma_f32 v[212:213], v[158:159], v[128:129], v[212:213]
	v_add_f32_e32 v210, v210, v211
	v_add_f32_e32 v212, v212, v213
	v_pk_mul_f32 v[214:215], v[232:233], v[208:209] op_sel_hi:[1,0]
	v_add_f32_dpp v210, v210, v210 quad_perm:[1,0,3,2] row_mask:0xf bank_mask:0xf bound_ctrl:1
	v_add_f32_dpp v212, v212, v212 quad_perm:[1,0,3,2] row_mask:0xf bank_mask:0xf bound_ctrl:1
	v_pk_mul_f32 v[216:217], v[234:235], v[208:209] op_sel_hi:[1,0]
	v_add_f32_dpp v210, v210, v210 quad_perm:[2,3,0,1] row_mask:0xf bank_mask:0xf bound_ctrl:1
	v_add_f32_dpp v212, v212, v212 quad_perm:[2,3,0,1] row_mask:0xf bank_mask:0xf bound_ctrl:1
	ds_read_b128 v[114:117], v197 offset:5392
	v_add_f32_dpp v210, v210, v210 row_half_mirror row_mask:0xf bank_mask:0xf bound_ctrl:1
	v_add_f32_dpp v212, v212, v212 row_half_mirror row_mask:0xf bank_mask:0xf bound_ctrl:1
	ds_read_b128 v[122:125], v197 offset:5424
	v_add_f32_dpp v218, v210, v210 row_mirror row_mask:0xf bank_mask:0xf bound_ctrl:1
	v_add_f32_dpp v240, v212, v212 row_mirror row_mask:0xf bank_mask:0xf bound_ctrl:1
	ds_read_b32 v206, v198 offset:6656
	v_pk_fma_f32 v[214:215], v[218:219], v[228:229], v[214:215] op_sel_hi:[0,1,1]
	v_pk_fma_f32 v[216:217], v[218:219], v[230:231], v[216:217] op_sel_hi:[0,1,1]
	v_cndmask_b32_e64 v241, v241, v240, s[6:7]
	v_pk_fma_f32 v[156:157], v[156:157], v[220:221], v[214:215]
	v_pk_fma_f32 v[158:159], v[158:159], v[222:223], v[216:217]
	ds_read_b128 v[118:121], v197 offset:5408
	ds_read_b128 v[110:113], v197 offset:5376
	ds_read_b128 v[126:129], v197 offset:5440
	s_waitcnt lgkmcnt(6)
	v_pk_mul_f32 v[210:211], v[156:157], v[94:95]
	v_pk_mul_f32 v[212:213], v[236:237], v[156:157]
	v_pk_fma_f32 v[210:211], v[158:159], v[96:97], v[210:211]
	v_pk_fma_f32 v[212:213], v[158:159], v[238:239], v[212:213]
	v_add_f32_e32 v210, v210, v211
	v_add_f32_e32 v212, v212, v213
	v_pk_mul_f32 v[214:215], v[102:103], v[204:205] op_sel_hi:[1,0]
	v_add_f32_dpp v210, v210, v210 quad_perm:[1,0,3,2] row_mask:0xf bank_mask:0xf bound_ctrl:1
	v_add_f32_dpp v212, v212, v212 quad_perm:[1,0,3,2] row_mask:0xf bank_mask:0xf bound_ctrl:1
	v_pk_mul_f32 v[216:217], v[104:105], v[204:205] op_sel_hi:[1,0]
	v_add_f32_dpp v210, v210, v210 quad_perm:[2,3,0,1] row_mask:0xf bank_mask:0xf bound_ctrl:1
	v_add_f32_dpp v212, v212, v212 quad_perm:[2,3,0,1] row_mask:0xf bank_mask:0xf bound_ctrl:1
	ds_read_b128 v[224:227], v197 offset:6736
	v_add_f32_dpp v210, v210, v210 row_half_mirror row_mask:0xf bank_mask:0xf bound_ctrl:1
	v_add_f32_dpp v212, v212, v212 row_half_mirror row_mask:0xf bank_mask:0xf bound_ctrl:1
	ds_read_b128 v[232:235], v197 offset:6768
	v_add_f32_dpp v218, v210, v210 row_mirror row_mask:0xf bank_mask:0xf bound_ctrl:1
	v_add_f32_dpp v240, v212, v212 row_mirror row_mask:0xf bank_mask:0xf bound_ctrl:1
	ds_read_b32 v208, v198 offset:8000
	v_pk_fma_f32 v[214:215], v[218:219], v[98:99], v[214:215] op_sel_hi:[0,1,1]
	v_pk_fma_f32 v[216:217], v[218:219], v[100:101], v[216:217] op_sel_hi:[0,1,1]
	v_cndmask_b32_e64 v241, v241, v240, s[8:9]
	v_pk_fma_f32 v[156:157], v[156:157], v[90:91], v[214:215]
	v_pk_fma_f32 v[158:159], v[158:159], v[92:93], v[216:217]
	ds_read_b128 v[228:231], v197 offset:6752
	ds_read_b128 v[220:223], v197 offset:6720
	ds_read_b128 v[236:239], v197 offset:6784
	s_waitcnt lgkmcnt(6)
	v_pk_mul_f32 v[210:211], v[156:157], v[114:115]
	v_pk_mul_f32 v[212:213], v[106:107], v[156:157]
	v_pk_fma_f32 v[210:211], v[158:159], v[116:117], v[210:211]
	v_pk_fma_f32 v[212:213], v[158:159], v[108:109], v[212:213]
	v_add_f32_e32 v210, v210, v211
	v_add_f32_e32 v212, v212, v213
	v_pk_mul_f32 v[214:215], v[122:123], v[206:207] op_sel_hi:[1,0]
	v_add_f32_dpp v210, v210, v210 quad_perm:[1,0,3,2] row_mask:0xf bank_mask:0xf bound_ctrl:1
	v_add_f32_dpp v212, v212, v212 quad_perm:[1,0,3,2] row_mask:0xf bank_mask:0xf bound_ctrl:1
	v_pk_mul_f32 v[216:217], v[124:125], v[206:207] op_sel_hi:[1,0]
	v_add_f32_dpp v210, v210, v210 quad_perm:[2,3,0,1] row_mask:0xf bank_mask:0xf bound_ctrl:1
	v_add_f32_dpp v212, v212, v212 quad_perm:[2,3,0,1] row_mask:0xf bank_mask:0xf bound_ctrl:1
	ds_read_b128 v[94:97], v197 offset:8080
	v_add_f32_dpp v210, v210, v210 row_half_mirror row_mask:0xf bank_mask:0xf bound_ctrl:1
	v_add_f32_dpp v212, v212, v212 row_half_mirror row_mask:0xf bank_mask:0xf bound_ctrl:1
	ds_read_b128 v[102:105], v197 offset:8112
	v_add_f32_dpp v218, v210, v210 row_mirror row_mask:0xf bank_mask:0xf bound_ctrl:1
	v_add_f32_dpp v240, v212, v212 row_mirror row_mask:0xf bank_mask:0xf bound_ctrl:1
	ds_read_b32 v204, v198 offset:9344
	v_pk_fma_f32 v[214:215], v[218:219], v[118:119], v[214:215] op_sel_hi:[0,1,1]
	v_pk_fma_f32 v[216:217], v[218:219], v[120:121], v[216:217] op_sel_hi:[0,1,1]
	v_cndmask_b32_e64 v241, v241, v240, s[10:11]
	v_pk_fma_f32 v[156:157], v[156:157], v[110:111], v[214:215]
	v_pk_fma_f32 v[158:159], v[158:159], v[112:113], v[216:217]
	ds_read_b128 v[98:101], v197 offset:8096
	ds_read_b128 v[90:93], v197 offset:8064
	ds_read_b128 v[106:109], v197 offset:8128
	s_waitcnt lgkmcnt(6)
	v_pk_mul_f32 v[210:211], v[156:157], v[224:225]
	v_pk_mul_f32 v[212:213], v[126:127], v[156:157]
	v_pk_fma_f32 v[210:211], v[158:159], v[226:227], v[210:211]
	v_pk_fma_f32 v[212:213], v[158:159], v[128:129], v[212:213]
	v_add_f32_e32 v210, v210, v211
	v_add_f32_e32 v212, v212, v213
	v_pk_mul_f32 v[214:215], v[232:233], v[208:209] op_sel_hi:[1,0]
	v_add_f32_dpp v210, v210, v210 quad_perm:[1,0,3,2] row_mask:0xf bank_mask:0xf bound_ctrl:1
	v_add_f32_dpp v212, v212, v212 quad_perm:[1,0,3,2] row_mask:0xf bank_mask:0xf bound_ctrl:1
	v_pk_mul_f32 v[216:217], v[234:235], v[208:209] op_sel_hi:[1,0]
	v_add_f32_dpp v210, v210, v210 quad_perm:[2,3,0,1] row_mask:0xf bank_mask:0xf bound_ctrl:1
	v_add_f32_dpp v212, v212, v212 quad_perm:[2,3,0,1] row_mask:0xf bank_mask:0xf bound_ctrl:1
	ds_read_b128 v[114:117], v197 offset:9424
	v_add_f32_dpp v210, v210, v210 row_half_mirror row_mask:0xf bank_mask:0xf bound_ctrl:1
	v_add_f32_dpp v212, v212, v212 row_half_mirror row_mask:0xf bank_mask:0xf bound_ctrl:1
	ds_read_b128 v[122:125], v197 offset:9456
	v_add_f32_dpp v218, v210, v210 row_mirror row_mask:0xf bank_mask:0xf bound_ctrl:1
	v_add_f32_dpp v240, v212, v212 row_mirror row_mask:0xf bank_mask:0xf bound_ctrl:1
	ds_read_b32 v206, v198 offset:10688
	v_pk_fma_f32 v[214:215], v[218:219], v[228:229], v[214:215] op_sel_hi:[0,1,1]
	v_pk_fma_f32 v[216:217], v[218:219], v[230:231], v[216:217] op_sel_hi:[0,1,1]
	v_cndmask_b32_e64 v241, v241, v240, s[12:13]
	v_pk_fma_f32 v[156:157], v[156:157], v[220:221], v[214:215]
	v_pk_fma_f32 v[158:159], v[158:159], v[222:223], v[216:217]
	ds_read_b128 v[118:121], v197 offset:9440
	ds_read_b128 v[110:113], v197 offset:9408
	ds_read_b128 v[126:129], v197 offset:9472
	s_waitcnt lgkmcnt(6)
	v_pk_mul_f32 v[210:211], v[156:157], v[94:95]
	v_pk_mul_f32 v[212:213], v[236:237], v[156:157]
	v_pk_fma_f32 v[210:211], v[158:159], v[96:97], v[210:211]
	v_pk_fma_f32 v[212:213], v[158:159], v[238:239], v[212:213]
	v_add_f32_e32 v210, v210, v211
	v_add_f32_e32 v212, v212, v213
	v_pk_mul_f32 v[214:215], v[102:103], v[204:205] op_sel_hi:[1,0]
	v_add_f32_dpp v210, v210, v210 quad_perm:[1,0,3,2] row_mask:0xf bank_mask:0xf bound_ctrl:1
	v_add_f32_dpp v212, v212, v212 quad_perm:[1,0,3,2] row_mask:0xf bank_mask:0xf bound_ctrl:1
	v_pk_mul_f32 v[216:217], v[104:105], v[204:205] op_sel_hi:[1,0]
	v_add_f32_dpp v210, v210, v210 quad_perm:[2,3,0,1] row_mask:0xf bank_mask:0xf bound_ctrl:1
	v_add_f32_dpp v212, v212, v212 quad_perm:[2,3,0,1] row_mask:0xf bank_mask:0xf bound_ctrl:1
	ds_read_b128 v[224:227], v197 offset:10768
	v_add_f32_dpp v210, v210, v210 row_half_mirror row_mask:0xf bank_mask:0xf bound_ctrl:1
	v_add_f32_dpp v212, v212, v212 row_half_mirror row_mask:0xf bank_mask:0xf bound_ctrl:1
	ds_read_b128 v[232:235], v197 offset:10800
	v_add_f32_dpp v218, v210, v210 row_mirror row_mask:0xf bank_mask:0xf bound_ctrl:1
	v_add_f32_dpp v240, v212, v212 row_mirror row_mask:0xf bank_mask:0xf bound_ctrl:1
	ds_read_b32 v208, v198 offset:12032
	v_pk_fma_f32 v[214:215], v[218:219], v[98:99], v[214:215] op_sel_hi:[0,1,1]
	v_pk_fma_f32 v[216:217], v[218:219], v[100:101], v[216:217] op_sel_hi:[0,1,1]
	v_cndmask_b32_e64 v241, v241, v240, s[14:15]
	v_pk_fma_f32 v[156:157], v[156:157], v[90:91], v[214:215]
	v_pk_fma_f32 v[158:159], v[158:159], v[92:93], v[216:217]
	ds_read_b128 v[228:231], v197 offset:10784
	ds_read_b128 v[220:223], v197 offset:10752
	ds_read_b128 v[236:239], v197 offset:10816
	s_waitcnt lgkmcnt(6)
	v_pk_mul_f32 v[210:211], v[156:157], v[114:115]
	v_pk_mul_f32 v[212:213], v[106:107], v[156:157]
	v_pk_fma_f32 v[210:211], v[158:159], v[116:117], v[210:211]
	v_pk_fma_f32 v[212:213], v[158:159], v[108:109], v[212:213]
	v_add_f32_e32 v210, v210, v211
	v_add_f32_e32 v212, v212, v213
	v_pk_mul_f32 v[214:215], v[122:123], v[206:207] op_sel_hi:[1,0]
	v_add_f32_dpp v210, v210, v210 quad_perm:[1,0,3,2] row_mask:0xf bank_mask:0xf bound_ctrl:1
	v_add_f32_dpp v212, v212, v212 quad_perm:[1,0,3,2] row_mask:0xf bank_mask:0xf bound_ctrl:1
	v_pk_mul_f32 v[216:217], v[124:125], v[206:207] op_sel_hi:[1,0]
	v_add_f32_dpp v210, v210, v210 quad_perm:[2,3,0,1] row_mask:0xf bank_mask:0xf bound_ctrl:1
	v_add_f32_dpp v212, v212, v212 quad_perm:[2,3,0,1] row_mask:0xf bank_mask:0xf bound_ctrl:1
	ds_read_b128 v[94:97], v197 offset:12112
	v_add_f32_dpp v210, v210, v210 row_half_mirror row_mask:0xf bank_mask:0xf bound_ctrl:1
	v_add_f32_dpp v212, v212, v212 row_half_mirror row_mask:0xf bank_mask:0xf bound_ctrl:1
	ds_read_b128 v[102:105], v197 offset:12144
	v_add_f32_dpp v218, v210, v210 row_mirror row_mask:0xf bank_mask:0xf bound_ctrl:1
	v_add_f32_dpp v240, v212, v212 row_mirror row_mask:0xf bank_mask:0xf bound_ctrl:1
	ds_read_b32 v204, v198 offset:13376
	v_pk_fma_f32 v[214:215], v[218:219], v[118:119], v[214:215] op_sel_hi:[0,1,1]
	v_pk_fma_f32 v[216:217], v[218:219], v[120:121], v[216:217] op_sel_hi:[0,1,1]
	v_cndmask_b32_e64 v241, v241, v240, s[16:17]
	v_pk_fma_f32 v[156:157], v[156:157], v[110:111], v[214:215]
	v_pk_fma_f32 v[158:159], v[158:159], v[112:113], v[216:217]
	ds_read_b128 v[98:101], v197 offset:12128
	ds_read_b128 v[90:93], v197 offset:12096
	ds_read_b128 v[106:109], v197 offset:12160
	s_waitcnt lgkmcnt(6)
	v_pk_mul_f32 v[210:211], v[156:157], v[224:225]
	v_pk_mul_f32 v[212:213], v[126:127], v[156:157]
	v_pk_fma_f32 v[210:211], v[158:159], v[226:227], v[210:211]
	v_pk_fma_f32 v[212:213], v[158:159], v[128:129], v[212:213]
	v_add_f32_e32 v210, v210, v211
	v_add_f32_e32 v212, v212, v213
	v_pk_mul_f32 v[214:215], v[232:233], v[208:209] op_sel_hi:[1,0]
	v_add_f32_dpp v210, v210, v210 quad_perm:[1,0,3,2] row_mask:0xf bank_mask:0xf bound_ctrl:1
	v_add_f32_dpp v212, v212, v212 quad_perm:[1,0,3,2] row_mask:0xf bank_mask:0xf bound_ctrl:1
	v_pk_mul_f32 v[216:217], v[234:235], v[208:209] op_sel_hi:[1,0]
	v_add_f32_dpp v210, v210, v210 quad_perm:[2,3,0,1] row_mask:0xf bank_mask:0xf bound_ctrl:1
	v_add_f32_dpp v212, v212, v212 quad_perm:[2,3,0,1] row_mask:0xf bank_mask:0xf bound_ctrl:1
	ds_read_b128 v[114:117], v197 offset:13456
	v_add_f32_dpp v210, v210, v210 row_half_mirror row_mask:0xf bank_mask:0xf bound_ctrl:1
	v_add_f32_dpp v212, v212, v212 row_half_mirror row_mask:0xf bank_mask:0xf bound_ctrl:1
	ds_read_b128 v[122:125], v197 offset:13488
	v_add_f32_dpp v218, v210, v210 row_mirror row_mask:0xf bank_mask:0xf bound_ctrl:1
	v_add_f32_dpp v240, v212, v212 row_mirror row_mask:0xf bank_mask:0xf bound_ctrl:1
	ds_read_b32 v206, v198 offset:14720
	v_pk_fma_f32 v[214:215], v[218:219], v[228:229], v[214:215] op_sel_hi:[0,1,1]
	v_pk_fma_f32 v[216:217], v[218:219], v[230:231], v[216:217] op_sel_hi:[0,1,1]
	v_cndmask_b32_e64 v241, v241, v240, s[18:19]
	v_pk_fma_f32 v[156:157], v[156:157], v[220:221], v[214:215]
	v_pk_fma_f32 v[158:159], v[158:159], v[222:223], v[216:217]
	ds_read_b128 v[118:121], v197 offset:13472
	ds_read_b128 v[110:113], v197 offset:13440
	ds_read_b128 v[126:129], v197 offset:13504
	s_waitcnt lgkmcnt(6)
	v_pk_mul_f32 v[210:211], v[156:157], v[94:95]
	v_pk_mul_f32 v[212:213], v[236:237], v[156:157]
	v_pk_fma_f32 v[210:211], v[158:159], v[96:97], v[210:211]
	v_pk_fma_f32 v[212:213], v[158:159], v[238:239], v[212:213]
	v_add_f32_e32 v210, v210, v211
	v_add_f32_e32 v212, v212, v213
	v_pk_mul_f32 v[214:215], v[102:103], v[204:205] op_sel_hi:[1,0]
	v_add_f32_dpp v210, v210, v210 quad_perm:[1,0,3,2] row_mask:0xf bank_mask:0xf bound_ctrl:1
	v_add_f32_dpp v212, v212, v212 quad_perm:[1,0,3,2] row_mask:0xf bank_mask:0xf bound_ctrl:1
	v_pk_mul_f32 v[216:217], v[104:105], v[204:205] op_sel_hi:[1,0]
	v_add_f32_dpp v210, v210, v210 quad_perm:[2,3,0,1] row_mask:0xf bank_mask:0xf bound_ctrl:1
	v_add_f32_dpp v212, v212, v212 quad_perm:[2,3,0,1] row_mask:0xf bank_mask:0xf bound_ctrl:1
	ds_read_b128 v[224:227], v197 offset:14800
	v_add_f32_dpp v210, v210, v210 row_half_mirror row_mask:0xf bank_mask:0xf bound_ctrl:1
	v_add_f32_dpp v212, v212, v212 row_half_mirror row_mask:0xf bank_mask:0xf bound_ctrl:1
	ds_read_b128 v[232:235], v197 offset:14832
	v_add_f32_dpp v218, v210, v210 row_mirror row_mask:0xf bank_mask:0xf bound_ctrl:1
	v_add_f32_dpp v240, v212, v212 row_mirror row_mask:0xf bank_mask:0xf bound_ctrl:1
	ds_read_b32 v208, v198 offset:16064
	v_pk_fma_f32 v[214:215], v[218:219], v[98:99], v[214:215] op_sel_hi:[0,1,1]
	v_pk_fma_f32 v[216:217], v[218:219], v[100:101], v[216:217] op_sel_hi:[0,1,1]
	v_cndmask_b32_e64 v241, v241, v240, s[20:21]
	v_pk_fma_f32 v[156:157], v[156:157], v[90:91], v[214:215]
	v_pk_fma_f32 v[158:159], v[158:159], v[92:93], v[216:217]
	ds_read_b128 v[228:231], v197 offset:14816
	ds_read_b128 v[220:223], v197 offset:14784
	ds_read_b128 v[236:239], v197 offset:14848
	s_waitcnt lgkmcnt(6)
	v_pk_mul_f32 v[210:211], v[156:157], v[114:115]
	v_pk_mul_f32 v[212:213], v[106:107], v[156:157]
	v_pk_fma_f32 v[210:211], v[158:159], v[116:117], v[210:211]
	v_pk_fma_f32 v[212:213], v[158:159], v[108:109], v[212:213]
	v_add_f32_e32 v210, v210, v211
	v_add_f32_e32 v212, v212, v213
	v_pk_mul_f32 v[214:215], v[122:123], v[206:207] op_sel_hi:[1,0]
	v_add_f32_dpp v210, v210, v210 quad_perm:[1,0,3,2] row_mask:0xf bank_mask:0xf bound_ctrl:1
	v_add_f32_dpp v212, v212, v212 quad_perm:[1,0,3,2] row_mask:0xf bank_mask:0xf bound_ctrl:1
	v_pk_mul_f32 v[216:217], v[124:125], v[206:207] op_sel_hi:[1,0]
	v_add_f32_dpp v210, v210, v210 quad_perm:[2,3,0,1] row_mask:0xf bank_mask:0xf bound_ctrl:1
	v_add_f32_dpp v212, v212, v212 quad_perm:[2,3,0,1] row_mask:0xf bank_mask:0xf bound_ctrl:1
	ds_read_b128 v[94:97], v197 offset:16144
	v_add_f32_dpp v210, v210, v210 row_half_mirror row_mask:0xf bank_mask:0xf bound_ctrl:1
	v_add_f32_dpp v212, v212, v212 row_half_mirror row_mask:0xf bank_mask:0xf bound_ctrl:1
	ds_read_b128 v[102:105], v197 offset:16176
	v_add_f32_dpp v218, v210, v210 row_mirror row_mask:0xf bank_mask:0xf bound_ctrl:1
	v_add_f32_dpp v240, v212, v212 row_mirror row_mask:0xf bank_mask:0xf bound_ctrl:1
	ds_read_b32 v204, v198 offset:17408
	v_pk_fma_f32 v[214:215], v[218:219], v[118:119], v[214:215] op_sel_hi:[0,1,1]
	v_pk_fma_f32 v[216:217], v[218:219], v[120:121], v[216:217] op_sel_hi:[0,1,1]
	v_cndmask_b32_e64 v241, v241, v240, s[22:23]
	v_pk_fma_f32 v[156:157], v[156:157], v[110:111], v[214:215]
	v_pk_fma_f32 v[158:159], v[158:159], v[112:113], v[216:217]
	ds_read_b128 v[98:101], v197 offset:16160
	ds_read_b128 v[90:93], v197 offset:16128
	ds_read_b128 v[106:109], v197 offset:16192
	s_waitcnt lgkmcnt(6)
	v_pk_mul_f32 v[210:211], v[156:157], v[224:225]
	v_pk_mul_f32 v[212:213], v[126:127], v[156:157]
	v_pk_fma_f32 v[210:211], v[158:159], v[226:227], v[210:211]
	v_pk_fma_f32 v[212:213], v[158:159], v[128:129], v[212:213]
	v_add_f32_e32 v210, v210, v211
	v_add_f32_e32 v212, v212, v213
	v_pk_mul_f32 v[214:215], v[232:233], v[208:209] op_sel_hi:[1,0]
	v_add_f32_dpp v210, v210, v210 quad_perm:[1,0,3,2] row_mask:0xf bank_mask:0xf bound_ctrl:1
	v_add_f32_dpp v212, v212, v212 quad_perm:[1,0,3,2] row_mask:0xf bank_mask:0xf bound_ctrl:1
	v_pk_mul_f32 v[216:217], v[234:235], v[208:209] op_sel_hi:[1,0]
	v_add_f32_dpp v210, v210, v210 quad_perm:[2,3,0,1] row_mask:0xf bank_mask:0xf bound_ctrl:1
	v_add_f32_dpp v212, v212, v212 quad_perm:[2,3,0,1] row_mask:0xf bank_mask:0xf bound_ctrl:1
	ds_read_b128 v[114:117], v197 offset:17488
	v_add_f32_dpp v210, v210, v210 row_half_mirror row_mask:0xf bank_mask:0xf bound_ctrl:1
	v_add_f32_dpp v212, v212, v212 row_half_mirror row_mask:0xf bank_mask:0xf bound_ctrl:1
	ds_read_b128 v[122:125], v197 offset:17520
	v_add_f32_dpp v218, v210, v210 row_mirror row_mask:0xf bank_mask:0xf bound_ctrl:1
	v_add_f32_dpp v240, v212, v212 row_mirror row_mask:0xf bank_mask:0xf bound_ctrl:1
	ds_read_b32 v206, v198 offset:18752
	v_pk_fma_f32 v[214:215], v[218:219], v[228:229], v[214:215] op_sel_hi:[0,1,1]
	v_pk_fma_f32 v[216:217], v[218:219], v[230:231], v[216:217] op_sel_hi:[0,1,1]
	v_cndmask_b32_e64 v241, v241, v240, s[24:25]
	v_pk_fma_f32 v[156:157], v[156:157], v[220:221], v[214:215]
	v_pk_fma_f32 v[158:159], v[158:159], v[222:223], v[216:217]
	ds_read_b128 v[118:121], v197 offset:17504
	ds_read_b128 v[110:113], v197 offset:17472
	ds_read_b128 v[126:129], v197 offset:17536
	s_waitcnt lgkmcnt(6)
	v_pk_mul_f32 v[210:211], v[156:157], v[94:95]
	v_pk_mul_f32 v[212:213], v[236:237], v[156:157]
	v_pk_fma_f32 v[210:211], v[158:159], v[96:97], v[210:211]
	v_pk_fma_f32 v[212:213], v[158:159], v[238:239], v[212:213]
	v_add_f32_e32 v210, v210, v211
	v_add_f32_e32 v212, v212, v213
	v_pk_mul_f32 v[214:215], v[102:103], v[204:205] op_sel_hi:[1,0]
	v_add_f32_dpp v210, v210, v210 quad_perm:[1,0,3,2] row_mask:0xf bank_mask:0xf bound_ctrl:1
	v_add_f32_dpp v212, v212, v212 quad_perm:[1,0,3,2] row_mask:0xf bank_mask:0xf bound_ctrl:1
	v_pk_mul_f32 v[216:217], v[104:105], v[204:205] op_sel_hi:[1,0]
	v_add_f32_dpp v210, v210, v210 quad_perm:[2,3,0,1] row_mask:0xf bank_mask:0xf bound_ctrl:1
	v_add_f32_dpp v212, v212, v212 quad_perm:[2,3,0,1] row_mask:0xf bank_mask:0xf bound_ctrl:1
	ds_read_b128 v[224:227], v197 offset:18832
	v_add_f32_dpp v210, v210, v210 row_half_mirror row_mask:0xf bank_mask:0xf bound_ctrl:1
	v_add_f32_dpp v212, v212, v212 row_half_mirror row_mask:0xf bank_mask:0xf bound_ctrl:1
	ds_read_b128 v[232:235], v197 offset:18864
	v_add_f32_dpp v218, v210, v210 row_mirror row_mask:0xf bank_mask:0xf bound_ctrl:1
	v_add_f32_dpp v240, v212, v212 row_mirror row_mask:0xf bank_mask:0xf bound_ctrl:1
	ds_read_b32 v208, v198 offset:20096
	v_pk_fma_f32 v[214:215], v[218:219], v[98:99], v[214:215] op_sel_hi:[0,1,1]
	v_pk_fma_f32 v[216:217], v[218:219], v[100:101], v[216:217] op_sel_hi:[0,1,1]
	v_cndmask_b32_e64 v241, v241, v240, s[26:27]
	v_pk_fma_f32 v[156:157], v[156:157], v[90:91], v[214:215]
	v_pk_fma_f32 v[158:159], v[158:159], v[92:93], v[216:217]
	ds_read_b128 v[228:231], v197 offset:18848
	ds_read_b128 v[220:223], v197 offset:18816
	ds_read_b128 v[236:239], v197 offset:18880
	s_waitcnt lgkmcnt(6)
	v_pk_mul_f32 v[210:211], v[156:157], v[114:115]
	v_pk_mul_f32 v[212:213], v[106:107], v[156:157]
	v_pk_fma_f32 v[210:211], v[158:159], v[116:117], v[210:211]
	v_pk_fma_f32 v[212:213], v[158:159], v[108:109], v[212:213]
	v_add_f32_e32 v210, v210, v211
	v_add_f32_e32 v212, v212, v213
	v_pk_mul_f32 v[214:215], v[122:123], v[206:207] op_sel_hi:[1,0]
	v_add_f32_dpp v210, v210, v210 quad_perm:[1,0,3,2] row_mask:0xf bank_mask:0xf bound_ctrl:1
	v_add_f32_dpp v212, v212, v212 quad_perm:[1,0,3,2] row_mask:0xf bank_mask:0xf bound_ctrl:1
	v_pk_mul_f32 v[216:217], v[124:125], v[206:207] op_sel_hi:[1,0]
	v_add_f32_dpp v210, v210, v210 quad_perm:[2,3,0,1] row_mask:0xf bank_mask:0xf bound_ctrl:1
	v_add_f32_dpp v212, v212, v212 quad_perm:[2,3,0,1] row_mask:0xf bank_mask:0xf bound_ctrl:1
	ds_read_b128 v[94:97], v197 offset:20176
	v_add_f32_dpp v210, v210, v210 row_half_mirror row_mask:0xf bank_mask:0xf bound_ctrl:1
	v_add_f32_dpp v212, v212, v212 row_half_mirror row_mask:0xf bank_mask:0xf bound_ctrl:1
	ds_read_b128 v[102:105], v197 offset:20208
	v_add_f32_dpp v218, v210, v210 row_mirror row_mask:0xf bank_mask:0xf bound_ctrl:1
	v_add_f32_dpp v240, v212, v212 row_mirror row_mask:0xf bank_mask:0xf bound_ctrl:1
	ds_read_b32 v204, v198 offset:21440
	v_pk_fma_f32 v[214:215], v[218:219], v[118:119], v[214:215] op_sel_hi:[0,1,1]
	v_pk_fma_f32 v[216:217], v[218:219], v[120:121], v[216:217] op_sel_hi:[0,1,1]
	v_cndmask_b32_e64 v241, v241, v240, s[28:29]
	v_pk_fma_f32 v[156:157], v[156:157], v[110:111], v[214:215]
	v_pk_fma_f32 v[158:159], v[158:159], v[112:113], v[216:217]
	ds_read_b128 v[98:101], v197 offset:20192
	ds_read_b128 v[90:93], v197 offset:20160
	ds_read_b128 v[106:109], v197 offset:20224
	s_waitcnt lgkmcnt(6)
	v_pk_mul_f32 v[210:211], v[156:157], v[224:225]
	v_pk_mul_f32 v[212:213], v[126:127], v[156:157]
	v_pk_fma_f32 v[210:211], v[158:159], v[226:227], v[210:211]
	v_pk_fma_f32 v[212:213], v[158:159], v[128:129], v[212:213]
	v_add_f32_e32 v210, v210, v211
	v_add_f32_e32 v212, v212, v213
	v_pk_mul_f32 v[214:215], v[232:233], v[208:209] op_sel_hi:[1,0]
	v_add_f32_dpp v210, v210, v210 quad_perm:[1,0,3,2] row_mask:0xf bank_mask:0xf bound_ctrl:1
	v_add_f32_dpp v212, v212, v212 quad_perm:[1,0,3,2] row_mask:0xf bank_mask:0xf bound_ctrl:1
	v_pk_mul_f32 v[216:217], v[234:235], v[208:209] op_sel_hi:[1,0]
	v_add_f32_dpp v210, v210, v210 quad_perm:[2,3,0,1] row_mask:0xf bank_mask:0xf bound_ctrl:1
	v_add_f32_dpp v212, v212, v212 quad_perm:[2,3,0,1] row_mask:0xf bank_mask:0xf bound_ctrl:1
	ds_read_b128 v[114:117], v197 offset:21520
	v_add_f32_dpp v210, v210, v210 row_half_mirror row_mask:0xf bank_mask:0xf bound_ctrl:1
	v_add_f32_dpp v212, v212, v212 row_half_mirror row_mask:0xf bank_mask:0xf bound_ctrl:1
	ds_read_b128 v[122:125], v197 offset:21552
	v_add_f32_dpp v218, v210, v210 row_mirror row_mask:0xf bank_mask:0xf bound_ctrl:1
	v_add_f32_dpp v240, v212, v212 row_mirror row_mask:0xf bank_mask:0xf bound_ctrl:1
	ds_read_b32 v206, v198 offset:22784
	v_pk_fma_f32 v[214:215], v[218:219], v[228:229], v[214:215] op_sel_hi:[0,1,1]
	v_pk_fma_f32 v[216:217], v[218:219], v[230:231], v[216:217] op_sel_hi:[0,1,1]
	v_cndmask_b32_e64 v241, v241, v240, s[30:31]
	v_pk_fma_f32 v[156:157], v[156:157], v[220:221], v[214:215]
	v_pk_fma_f32 v[158:159], v[158:159], v[222:223], v[216:217]
	ds_read_b128 v[118:121], v197 offset:21536
	ds_read_b128 v[110:113], v197 offset:21504
	ds_read_b128 v[126:129], v197 offset:21568
	s_waitcnt lgkmcnt(6)
	v_pk_mul_f32 v[210:211], v[156:157], v[94:95]
	v_pk_mul_f32 v[212:213], v[236:237], v[156:157]
	v_pk_fma_f32 v[210:211], v[158:159], v[96:97], v[210:211]
	v_pk_fma_f32 v[212:213], v[158:159], v[238:239], v[212:213]
	v_add_f32_e32 v210, v210, v211
	v_add_f32_e32 v212, v212, v213
	v_pk_mul_f32 v[214:215], v[102:103], v[204:205] op_sel_hi:[1,0]
	v_add_f32_dpp v210, v210, v210 quad_perm:[1,0,3,2] row_mask:0xf bank_mask:0xf bound_ctrl:1
	v_add_f32_dpp v212, v212, v212 quad_perm:[1,0,3,2] row_mask:0xf bank_mask:0xf bound_ctrl:1
	v_pk_mul_f32 v[216:217], v[104:105], v[204:205] op_sel_hi:[1,0]
	v_add_f32_dpp v210, v210, v210 quad_perm:[2,3,0,1] row_mask:0xf bank_mask:0xf bound_ctrl:1
	v_add_f32_dpp v212, v212, v212 quad_perm:[2,3,0,1] row_mask:0xf bank_mask:0xf bound_ctrl:1
	ds_read_b128 v[224:227], v197 offset:22864
	v_add_f32_dpp v210, v210, v210 row_half_mirror row_mask:0xf bank_mask:0xf bound_ctrl:1
	v_add_f32_dpp v212, v212, v212 row_half_mirror row_mask:0xf bank_mask:0xf bound_ctrl:1
	ds_read_b128 v[232:235], v197 offset:22896
	v_add_f32_dpp v218, v210, v210 row_mirror row_mask:0xf bank_mask:0xf bound_ctrl:1
	v_add_f32_dpp v240, v212, v212 row_mirror row_mask:0xf bank_mask:0xf bound_ctrl:1
	ds_read_b32 v208, v198 offset:24128
	v_pk_fma_f32 v[214:215], v[218:219], v[98:99], v[214:215] op_sel_hi:[0,1,1]
	v_pk_fma_f32 v[216:217], v[218:219], v[100:101], v[216:217] op_sel_hi:[0,1,1]
	v_cndmask_b32_e64 v241, v241, v240, s[34:35]
	v_pk_fma_f32 v[156:157], v[156:157], v[90:91], v[214:215]
	v_pk_fma_f32 v[158:159], v[158:159], v[92:93], v[216:217]
	ds_read_b128 v[228:231], v197 offset:22880
	ds_read_b128 v[220:223], v197 offset:22848
	ds_read_b128 v[236:239], v197 offset:22912
	s_waitcnt lgkmcnt(6)
	v_pk_mul_f32 v[210:211], v[156:157], v[114:115]
	v_pk_mul_f32 v[212:213], v[106:107], v[156:157]
	v_pk_fma_f32 v[210:211], v[158:159], v[116:117], v[210:211]
	v_pk_fma_f32 v[212:213], v[158:159], v[108:109], v[212:213]
	v_add_f32_e32 v210, v210, v211
	v_add_f32_e32 v212, v212, v213
	v_pk_mul_f32 v[214:215], v[122:123], v[206:207] op_sel_hi:[1,0]
	v_add_f32_dpp v210, v210, v210 quad_perm:[1,0,3,2] row_mask:0xf bank_mask:0xf bound_ctrl:1
	v_add_f32_dpp v212, v212, v212 quad_perm:[1,0,3,2] row_mask:0xf bank_mask:0xf bound_ctrl:1
	v_pk_mul_f32 v[216:217], v[124:125], v[206:207] op_sel_hi:[1,0]
	v_add_f32_dpp v210, v210, v210 quad_perm:[2,3,0,1] row_mask:0xf bank_mask:0xf bound_ctrl:1
	v_add_f32_dpp v212, v212, v212 quad_perm:[2,3,0,1] row_mask:0xf bank_mask:0xf bound_ctrl:1
	ds_read_b128 v[94:97], v197 offset:24208
	v_add_f32_dpp v210, v210, v210 row_half_mirror row_mask:0xf bank_mask:0xf bound_ctrl:1
	v_add_f32_dpp v212, v212, v212 row_half_mirror row_mask:0xf bank_mask:0xf bound_ctrl:1
	ds_read_b128 v[102:105], v197 offset:24240
	v_add_f32_dpp v218, v210, v210 row_mirror row_mask:0xf bank_mask:0xf bound_ctrl:1
	v_add_f32_dpp v240, v212, v212 row_mirror row_mask:0xf bank_mask:0xf bound_ctrl:1
	ds_read_b32 v204, v198 offset:25472
	v_pk_fma_f32 v[214:215], v[218:219], v[118:119], v[214:215] op_sel_hi:[0,1,1]
	v_pk_fma_f32 v[216:217], v[218:219], v[120:121], v[216:217] op_sel_hi:[0,1,1]
	v_cndmask_b32_e64 v241, v241, v240, s[36:37]
	v_pk_fma_f32 v[156:157], v[156:157], v[110:111], v[214:215]
	v_pk_fma_f32 v[158:159], v[158:159], v[112:113], v[216:217]
	ds_read_b128 v[98:101], v197 offset:24224
	ds_read_b128 v[90:93], v197 offset:24192
	ds_read_b128 v[106:109], v197 offset:24256
	s_waitcnt lgkmcnt(6)
	v_pk_mul_f32 v[210:211], v[156:157], v[224:225]
	v_pk_mul_f32 v[212:213], v[126:127], v[156:157]
	v_pk_fma_f32 v[210:211], v[158:159], v[226:227], v[210:211]
	v_pk_fma_f32 v[212:213], v[158:159], v[128:129], v[212:213]
	v_add_f32_e32 v210, v210, v211
	v_add_f32_e32 v212, v212, v213
	v_pk_mul_f32 v[214:215], v[232:233], v[208:209] op_sel_hi:[1,0]
	v_add_f32_dpp v210, v210, v210 quad_perm:[1,0,3,2] row_mask:0xf bank_mask:0xf bound_ctrl:1
	v_add_f32_dpp v212, v212, v212 quad_perm:[1,0,3,2] row_mask:0xf bank_mask:0xf bound_ctrl:1
	v_pk_mul_f32 v[216:217], v[234:235], v[208:209] op_sel_hi:[1,0]
	v_add_f32_dpp v210, v210, v210 quad_perm:[2,3,0,1] row_mask:0xf bank_mask:0xf bound_ctrl:1
	v_add_f32_dpp v212, v212, v212 quad_perm:[2,3,0,1] row_mask:0xf bank_mask:0xf bound_ctrl:1
	ds_read_b128 v[114:117], v197 offset:25552
	v_add_f32_dpp v210, v210, v210 row_half_mirror row_mask:0xf bank_mask:0xf bound_ctrl:1
	v_add_f32_dpp v212, v212, v212 row_half_mirror row_mask:0xf bank_mask:0xf bound_ctrl:1
	ds_read_b128 v[122:125], v197 offset:25584
	v_add_f32_dpp v218, v210, v210 row_mirror row_mask:0xf bank_mask:0xf bound_ctrl:1
	v_add_f32_dpp v240, v212, v212 row_mirror row_mask:0xf bank_mask:0xf bound_ctrl:1
	ds_read_b32 v206, v198 offset:26816
	v_pk_fma_f32 v[214:215], v[218:219], v[228:229], v[214:215] op_sel_hi:[0,1,1]
	v_pk_fma_f32 v[216:217], v[218:219], v[230:231], v[216:217] op_sel_hi:[0,1,1]
	v_cndmask_b32_e64 v242, 0, v240, s[4:5]
	v_pk_fma_f32 v[156:157], v[156:157], v[220:221], v[214:215]
	v_pk_fma_f32 v[158:159], v[158:159], v[222:223], v[216:217]
	ds_read_b128 v[118:121], v197 offset:25568
	ds_read_b128 v[110:113], v197 offset:25536
	ds_read_b128 v[126:129], v197 offset:25600
	s_waitcnt lgkmcnt(6)
	v_pk_mul_f32 v[210:211], v[156:157], v[94:95]
	v_pk_mul_f32 v[212:213], v[236:237], v[156:157]
	v_pk_fma_f32 v[210:211], v[158:159], v[96:97], v[210:211]
	v_pk_fma_f32 v[212:213], v[158:159], v[238:239], v[212:213]
	v_add_f32_e32 v210, v210, v211
	v_add_f32_e32 v212, v212, v213
	v_pk_mul_f32 v[214:215], v[102:103], v[204:205] op_sel_hi:[1,0]
	v_add_f32_dpp v210, v210, v210 quad_perm:[1,0,3,2] row_mask:0xf bank_mask:0xf bound_ctrl:1
	v_add_f32_dpp v212, v212, v212 quad_perm:[1,0,3,2] row_mask:0xf bank_mask:0xf bound_ctrl:1
	v_pk_mul_f32 v[216:217], v[104:105], v[204:205] op_sel_hi:[1,0]
	v_add_f32_dpp v210, v210, v210 quad_perm:[2,3,0,1] row_mask:0xf bank_mask:0xf bound_ctrl:1
	v_add_f32_dpp v212, v212, v212 quad_perm:[2,3,0,1] row_mask:0xf bank_mask:0xf bound_ctrl:1
	ds_read_b128 v[224:227], v197 offset:26896
	v_add_f32_dpp v210, v210, v210 row_half_mirror row_mask:0xf bank_mask:0xf bound_ctrl:1
	v_add_f32_dpp v212, v212, v212 row_half_mirror row_mask:0xf bank_mask:0xf bound_ctrl:1
	ds_read_b128 v[232:235], v197 offset:26928
	v_add_f32_dpp v218, v210, v210 row_mirror row_mask:0xf bank_mask:0xf bound_ctrl:1
	v_add_f32_dpp v240, v212, v212 row_mirror row_mask:0xf bank_mask:0xf bound_ctrl:1
	ds_read_b32 v208, v198 offset:28160
	v_pk_fma_f32 v[214:215], v[218:219], v[98:99], v[214:215] op_sel_hi:[0,1,1]
	v_pk_fma_f32 v[216:217], v[218:219], v[100:101], v[216:217] op_sel_hi:[0,1,1]
	v_cndmask_b32_e64 v242, v242, v240, s[6:7]
	v_pk_fma_f32 v[156:157], v[156:157], v[90:91], v[214:215]
	v_pk_fma_f32 v[158:159], v[158:159], v[92:93], v[216:217]
	ds_read_b128 v[228:231], v197 offset:26912
	ds_read_b128 v[220:223], v197 offset:26880
	ds_read_b128 v[236:239], v197 offset:26944
	s_waitcnt lgkmcnt(6)
	v_pk_mul_f32 v[210:211], v[156:157], v[114:115]
	v_pk_mul_f32 v[212:213], v[106:107], v[156:157]
	v_pk_fma_f32 v[210:211], v[158:159], v[116:117], v[210:211]
	v_pk_fma_f32 v[212:213], v[158:159], v[108:109], v[212:213]
	v_add_f32_e32 v210, v210, v211
	v_add_f32_e32 v212, v212, v213
	v_pk_mul_f32 v[214:215], v[122:123], v[206:207] op_sel_hi:[1,0]
	v_add_f32_dpp v210, v210, v210 quad_perm:[1,0,3,2] row_mask:0xf bank_mask:0xf bound_ctrl:1
	v_add_f32_dpp v212, v212, v212 quad_perm:[1,0,3,2] row_mask:0xf bank_mask:0xf bound_ctrl:1
	v_pk_mul_f32 v[216:217], v[124:125], v[206:207] op_sel_hi:[1,0]
	v_add_f32_dpp v210, v210, v210 quad_perm:[2,3,0,1] row_mask:0xf bank_mask:0xf bound_ctrl:1
	v_add_f32_dpp v212, v212, v212 quad_perm:[2,3,0,1] row_mask:0xf bank_mask:0xf bound_ctrl:1
	ds_read_b128 v[94:97], v197 offset:28240
	v_add_f32_dpp v210, v210, v210 row_half_mirror row_mask:0xf bank_mask:0xf bound_ctrl:1
	v_add_f32_dpp v212, v212, v212 row_half_mirror row_mask:0xf bank_mask:0xf bound_ctrl:1
	ds_read_b128 v[102:105], v197 offset:28272
	v_add_f32_dpp v218, v210, v210 row_mirror row_mask:0xf bank_mask:0xf bound_ctrl:1
	v_add_f32_dpp v240, v212, v212 row_mirror row_mask:0xf bank_mask:0xf bound_ctrl:1
	ds_read_b32 v204, v198 offset:29504
	v_pk_fma_f32 v[214:215], v[218:219], v[118:119], v[214:215] op_sel_hi:[0,1,1]
	v_pk_fma_f32 v[216:217], v[218:219], v[120:121], v[216:217] op_sel_hi:[0,1,1]
	v_cndmask_b32_e64 v242, v242, v240, s[8:9]
	v_pk_fma_f32 v[156:157], v[156:157], v[110:111], v[214:215]
	v_pk_fma_f32 v[158:159], v[158:159], v[112:113], v[216:217]
	ds_read_b128 v[98:101], v197 offset:28256
	ds_read_b128 v[90:93], v197 offset:28224
	ds_read_b128 v[106:109], v197 offset:28288
	s_waitcnt lgkmcnt(6)
	v_pk_mul_f32 v[210:211], v[156:157], v[224:225]
	v_pk_mul_f32 v[212:213], v[126:127], v[156:157]
	v_pk_fma_f32 v[210:211], v[158:159], v[226:227], v[210:211]
	v_pk_fma_f32 v[212:213], v[158:159], v[128:129], v[212:213]
	v_add_f32_e32 v210, v210, v211
	v_add_f32_e32 v212, v212, v213
	v_pk_mul_f32 v[214:215], v[232:233], v[208:209] op_sel_hi:[1,0]
	v_add_f32_dpp v210, v210, v210 quad_perm:[1,0,3,2] row_mask:0xf bank_mask:0xf bound_ctrl:1
	v_add_f32_dpp v212, v212, v212 quad_perm:[1,0,3,2] row_mask:0xf bank_mask:0xf bound_ctrl:1
	v_pk_mul_f32 v[216:217], v[234:235], v[208:209] op_sel_hi:[1,0]
	v_add_f32_dpp v210, v210, v210 quad_perm:[2,3,0,1] row_mask:0xf bank_mask:0xf bound_ctrl:1
	v_add_f32_dpp v212, v212, v212 quad_perm:[2,3,0,1] row_mask:0xf bank_mask:0xf bound_ctrl:1
	ds_read_b128 v[114:117], v197 offset:29584
	v_add_f32_dpp v210, v210, v210 row_half_mirror row_mask:0xf bank_mask:0xf bound_ctrl:1
	v_add_f32_dpp v212, v212, v212 row_half_mirror row_mask:0xf bank_mask:0xf bound_ctrl:1
	ds_read_b128 v[122:125], v197 offset:29616
	v_add_f32_dpp v218, v210, v210 row_mirror row_mask:0xf bank_mask:0xf bound_ctrl:1
	v_add_f32_dpp v240, v212, v212 row_mirror row_mask:0xf bank_mask:0xf bound_ctrl:1
	ds_read_b32 v206, v198 offset:30848
	v_pk_fma_f32 v[214:215], v[218:219], v[228:229], v[214:215] op_sel_hi:[0,1,1]
	v_pk_fma_f32 v[216:217], v[218:219], v[230:231], v[216:217] op_sel_hi:[0,1,1]
	v_cndmask_b32_e64 v242, v242, v240, s[10:11]
	v_pk_fma_f32 v[156:157], v[156:157], v[220:221], v[214:215]
	v_pk_fma_f32 v[158:159], v[158:159], v[222:223], v[216:217]
	ds_read_b128 v[118:121], v197 offset:29600
	ds_read_b128 v[110:113], v197 offset:29568
	ds_read_b128 v[126:129], v197 offset:29632
	s_waitcnt lgkmcnt(6)
	v_pk_mul_f32 v[210:211], v[156:157], v[94:95]
	v_pk_mul_f32 v[212:213], v[236:237], v[156:157]
	v_pk_fma_f32 v[210:211], v[158:159], v[96:97], v[210:211]
	v_pk_fma_f32 v[212:213], v[158:159], v[238:239], v[212:213]
	v_add_f32_e32 v210, v210, v211
	v_add_f32_e32 v212, v212, v213
	v_pk_mul_f32 v[214:215], v[102:103], v[204:205] op_sel_hi:[1,0]
	v_add_f32_dpp v210, v210, v210 quad_perm:[1,0,3,2] row_mask:0xf bank_mask:0xf bound_ctrl:1
	v_add_f32_dpp v212, v212, v212 quad_perm:[1,0,3,2] row_mask:0xf bank_mask:0xf bound_ctrl:1
	v_pk_mul_f32 v[216:217], v[104:105], v[204:205] op_sel_hi:[1,0]
	v_add_f32_dpp v210, v210, v210 quad_perm:[2,3,0,1] row_mask:0xf bank_mask:0xf bound_ctrl:1
	v_add_f32_dpp v212, v212, v212 quad_perm:[2,3,0,1] row_mask:0xf bank_mask:0xf bound_ctrl:1
	ds_read_b128 v[224:227], v197 offset:30928
	v_add_f32_dpp v210, v210, v210 row_half_mirror row_mask:0xf bank_mask:0xf bound_ctrl:1
	v_add_f32_dpp v212, v212, v212 row_half_mirror row_mask:0xf bank_mask:0xf bound_ctrl:1
	ds_read_b128 v[232:235], v197 offset:30960
	v_add_f32_dpp v218, v210, v210 row_mirror row_mask:0xf bank_mask:0xf bound_ctrl:1
	v_add_f32_dpp v240, v212, v212 row_mirror row_mask:0xf bank_mask:0xf bound_ctrl:1
	ds_read_b32 v208, v198 offset:32192
	v_pk_fma_f32 v[214:215], v[218:219], v[98:99], v[214:215] op_sel_hi:[0,1,1]
	v_pk_fma_f32 v[216:217], v[218:219], v[100:101], v[216:217] op_sel_hi:[0,1,1]
	v_cndmask_b32_e64 v242, v242, v240, s[12:13]
	v_pk_fma_f32 v[156:157], v[156:157], v[90:91], v[214:215]
	v_pk_fma_f32 v[158:159], v[158:159], v[92:93], v[216:217]
	ds_read_b128 v[228:231], v197 offset:30944
	ds_read_b128 v[220:223], v197 offset:30912
	ds_read_b128 v[236:239], v197 offset:30976
	s_waitcnt lgkmcnt(6)
	v_pk_mul_f32 v[210:211], v[156:157], v[114:115]
	v_pk_mul_f32 v[212:213], v[106:107], v[156:157]
	v_pk_fma_f32 v[210:211], v[158:159], v[116:117], v[210:211]
	v_pk_fma_f32 v[212:213], v[158:159], v[108:109], v[212:213]
	v_add_f32_e32 v210, v210, v211
	v_add_f32_e32 v212, v212, v213
	v_pk_mul_f32 v[214:215], v[122:123], v[206:207] op_sel_hi:[1,0]
	v_add_f32_dpp v210, v210, v210 quad_perm:[1,0,3,2] row_mask:0xf bank_mask:0xf bound_ctrl:1
	v_add_f32_dpp v212, v212, v212 quad_perm:[1,0,3,2] row_mask:0xf bank_mask:0xf bound_ctrl:1
	v_pk_mul_f32 v[216:217], v[124:125], v[206:207] op_sel_hi:[1,0]
	v_add_f32_dpp v210, v210, v210 quad_perm:[2,3,0,1] row_mask:0xf bank_mask:0xf bound_ctrl:1
	v_add_f32_dpp v212, v212, v212 quad_perm:[2,3,0,1] row_mask:0xf bank_mask:0xf bound_ctrl:1
	ds_read_b128 v[94:97], v197 offset:32272
	v_add_f32_dpp v210, v210, v210 row_half_mirror row_mask:0xf bank_mask:0xf bound_ctrl:1
	v_add_f32_dpp v212, v212, v212 row_half_mirror row_mask:0xf bank_mask:0xf bound_ctrl:1
	ds_read_b128 v[102:105], v197 offset:32304
	v_add_f32_dpp v218, v210, v210 row_mirror row_mask:0xf bank_mask:0xf bound_ctrl:1
	v_add_f32_dpp v240, v212, v212 row_mirror row_mask:0xf bank_mask:0xf bound_ctrl:1
	ds_read_b32 v204, v198 offset:33536
	v_pk_fma_f32 v[214:215], v[218:219], v[118:119], v[214:215] op_sel_hi:[0,1,1]
	v_pk_fma_f32 v[216:217], v[218:219], v[120:121], v[216:217] op_sel_hi:[0,1,1]
	v_cndmask_b32_e64 v242, v242, v240, s[14:15]
	v_pk_fma_f32 v[156:157], v[156:157], v[110:111], v[214:215]
	v_pk_fma_f32 v[158:159], v[158:159], v[112:113], v[216:217]
	ds_read_b128 v[98:101], v197 offset:32288
	ds_read_b128 v[90:93], v197 offset:32256
	ds_read_b128 v[106:109], v197 offset:32320
	s_waitcnt lgkmcnt(6)
	v_pk_mul_f32 v[210:211], v[156:157], v[224:225]
	v_pk_mul_f32 v[212:213], v[126:127], v[156:157]
	v_pk_fma_f32 v[210:211], v[158:159], v[226:227], v[210:211]
	v_pk_fma_f32 v[212:213], v[158:159], v[128:129], v[212:213]
	v_add_f32_e32 v210, v210, v211
	v_add_f32_e32 v212, v212, v213
	v_pk_mul_f32 v[214:215], v[232:233], v[208:209] op_sel_hi:[1,0]
	v_add_f32_dpp v210, v210, v210 quad_perm:[1,0,3,2] row_mask:0xf bank_mask:0xf bound_ctrl:1
	v_add_f32_dpp v212, v212, v212 quad_perm:[1,0,3,2] row_mask:0xf bank_mask:0xf bound_ctrl:1
	v_pk_mul_f32 v[216:217], v[234:235], v[208:209] op_sel_hi:[1,0]
	v_add_f32_dpp v210, v210, v210 quad_perm:[2,3,0,1] row_mask:0xf bank_mask:0xf bound_ctrl:1
	v_add_f32_dpp v212, v212, v212 quad_perm:[2,3,0,1] row_mask:0xf bank_mask:0xf bound_ctrl:1
	ds_read_b128 v[114:117], v197 offset:33616
	v_add_f32_dpp v210, v210, v210 row_half_mirror row_mask:0xf bank_mask:0xf bound_ctrl:1
	v_add_f32_dpp v212, v212, v212 row_half_mirror row_mask:0xf bank_mask:0xf bound_ctrl:1
	ds_read_b128 v[122:125], v197 offset:33648
	v_add_f32_dpp v218, v210, v210 row_mirror row_mask:0xf bank_mask:0xf bound_ctrl:1
	v_add_f32_dpp v240, v212, v212 row_mirror row_mask:0xf bank_mask:0xf bound_ctrl:1
	ds_read_b32 v206, v198 offset:34880
	v_pk_fma_f32 v[214:215], v[218:219], v[228:229], v[214:215] op_sel_hi:[0,1,1]
	v_pk_fma_f32 v[216:217], v[218:219], v[230:231], v[216:217] op_sel_hi:[0,1,1]
	v_cndmask_b32_e64 v242, v242, v240, s[16:17]
	v_pk_fma_f32 v[156:157], v[156:157], v[220:221], v[214:215]
	v_pk_fma_f32 v[158:159], v[158:159], v[222:223], v[216:217]
	ds_read_b128 v[118:121], v197 offset:33632
	ds_read_b128 v[110:113], v197 offset:33600
	ds_read_b128 v[126:129], v197 offset:33664
	s_waitcnt lgkmcnt(6)
	v_pk_mul_f32 v[210:211], v[156:157], v[94:95]
	v_pk_mul_f32 v[212:213], v[236:237], v[156:157]
	v_pk_fma_f32 v[210:211], v[158:159], v[96:97], v[210:211]
	v_pk_fma_f32 v[212:213], v[158:159], v[238:239], v[212:213]
	v_add_f32_e32 v210, v210, v211
	v_add_f32_e32 v212, v212, v213
	v_pk_mul_f32 v[214:215], v[102:103], v[204:205] op_sel_hi:[1,0]
	v_add_f32_dpp v210, v210, v210 quad_perm:[1,0,3,2] row_mask:0xf bank_mask:0xf bound_ctrl:1
	v_add_f32_dpp v212, v212, v212 quad_perm:[1,0,3,2] row_mask:0xf bank_mask:0xf bound_ctrl:1
	v_pk_mul_f32 v[216:217], v[104:105], v[204:205] op_sel_hi:[1,0]
	v_add_f32_dpp v210, v210, v210 quad_perm:[2,3,0,1] row_mask:0xf bank_mask:0xf bound_ctrl:1
	v_add_f32_dpp v212, v212, v212 quad_perm:[2,3,0,1] row_mask:0xf bank_mask:0xf bound_ctrl:1
	ds_read_b128 v[224:227], v197 offset:34960
	v_add_f32_dpp v210, v210, v210 row_half_mirror row_mask:0xf bank_mask:0xf bound_ctrl:1
	v_add_f32_dpp v212, v212, v212 row_half_mirror row_mask:0xf bank_mask:0xf bound_ctrl:1
	ds_read_b128 v[232:235], v197 offset:34992
	v_add_f32_dpp v218, v210, v210 row_mirror row_mask:0xf bank_mask:0xf bound_ctrl:1
	v_add_f32_dpp v240, v212, v212 row_mirror row_mask:0xf bank_mask:0xf bound_ctrl:1
	ds_read_b32 v208, v198 offset:36224
	v_pk_fma_f32 v[214:215], v[218:219], v[98:99], v[214:215] op_sel_hi:[0,1,1]
	v_pk_fma_f32 v[216:217], v[218:219], v[100:101], v[216:217] op_sel_hi:[0,1,1]
	v_cndmask_b32_e64 v242, v242, v240, s[18:19]
	v_pk_fma_f32 v[156:157], v[156:157], v[90:91], v[214:215]
	v_pk_fma_f32 v[158:159], v[158:159], v[92:93], v[216:217]
	ds_read_b128 v[228:231], v197 offset:34976
	ds_read_b128 v[220:223], v197 offset:34944
	ds_read_b128 v[236:239], v197 offset:35008
	s_waitcnt lgkmcnt(6)
	v_pk_mul_f32 v[210:211], v[156:157], v[114:115]
	v_pk_mul_f32 v[212:213], v[106:107], v[156:157]
	v_pk_fma_f32 v[210:211], v[158:159], v[116:117], v[210:211]
	v_pk_fma_f32 v[212:213], v[158:159], v[108:109], v[212:213]
	v_add_f32_e32 v210, v210, v211
	v_add_f32_e32 v212, v212, v213
	v_pk_mul_f32 v[214:215], v[122:123], v[206:207] op_sel_hi:[1,0]
	v_add_f32_dpp v210, v210, v210 quad_perm:[1,0,3,2] row_mask:0xf bank_mask:0xf bound_ctrl:1
	v_add_f32_dpp v212, v212, v212 quad_perm:[1,0,3,2] row_mask:0xf bank_mask:0xf bound_ctrl:1
	v_pk_mul_f32 v[216:217], v[124:125], v[206:207] op_sel_hi:[1,0]
	v_add_f32_dpp v210, v210, v210 quad_perm:[2,3,0,1] row_mask:0xf bank_mask:0xf bound_ctrl:1
	v_add_f32_dpp v212, v212, v212 quad_perm:[2,3,0,1] row_mask:0xf bank_mask:0xf bound_ctrl:1
	ds_read_b128 v[94:97], v197 offset:36304
	v_add_f32_dpp v210, v210, v210 row_half_mirror row_mask:0xf bank_mask:0xf bound_ctrl:1
	v_add_f32_dpp v212, v212, v212 row_half_mirror row_mask:0xf bank_mask:0xf bound_ctrl:1
	ds_read_b128 v[102:105], v197 offset:36336
	v_add_f32_dpp v218, v210, v210 row_mirror row_mask:0xf bank_mask:0xf bound_ctrl:1
	v_add_f32_dpp v240, v212, v212 row_mirror row_mask:0xf bank_mask:0xf bound_ctrl:1
	ds_read_b32 v204, v198 offset:37568
	v_pk_fma_f32 v[214:215], v[218:219], v[118:119], v[214:215] op_sel_hi:[0,1,1]
	v_pk_fma_f32 v[216:217], v[218:219], v[120:121], v[216:217] op_sel_hi:[0,1,1]
	v_cndmask_b32_e64 v242, v242, v240, s[20:21]
	v_pk_fma_f32 v[156:157], v[156:157], v[110:111], v[214:215]
	v_pk_fma_f32 v[158:159], v[158:159], v[112:113], v[216:217]
	ds_read_b128 v[98:101], v197 offset:36320
	ds_read_b128 v[90:93], v197 offset:36288
	ds_read_b128 v[106:109], v197 offset:36352
	s_waitcnt lgkmcnt(6)
	v_pk_mul_f32 v[210:211], v[156:157], v[224:225]
	v_pk_mul_f32 v[212:213], v[126:127], v[156:157]
	v_pk_fma_f32 v[210:211], v[158:159], v[226:227], v[210:211]
	v_pk_fma_f32 v[212:213], v[158:159], v[128:129], v[212:213]
	v_add_f32_e32 v210, v210, v211
	v_add_f32_e32 v212, v212, v213
	v_pk_mul_f32 v[214:215], v[232:233], v[208:209] op_sel_hi:[1,0]
	v_add_f32_dpp v210, v210, v210 quad_perm:[1,0,3,2] row_mask:0xf bank_mask:0xf bound_ctrl:1
	v_add_f32_dpp v212, v212, v212 quad_perm:[1,0,3,2] row_mask:0xf bank_mask:0xf bound_ctrl:1
	v_pk_mul_f32 v[216:217], v[234:235], v[208:209] op_sel_hi:[1,0]
	v_add_f32_dpp v210, v210, v210 quad_perm:[2,3,0,1] row_mask:0xf bank_mask:0xf bound_ctrl:1
	v_add_f32_dpp v212, v212, v212 quad_perm:[2,3,0,1] row_mask:0xf bank_mask:0xf bound_ctrl:1
	ds_read_b128 v[114:117], v197 offset:37648
	v_add_f32_dpp v210, v210, v210 row_half_mirror row_mask:0xf bank_mask:0xf bound_ctrl:1
	v_add_f32_dpp v212, v212, v212 row_half_mirror row_mask:0xf bank_mask:0xf bound_ctrl:1
	ds_read_b128 v[122:125], v197 offset:37680
	v_add_f32_dpp v218, v210, v210 row_mirror row_mask:0xf bank_mask:0xf bound_ctrl:1
	v_add_f32_dpp v240, v212, v212 row_mirror row_mask:0xf bank_mask:0xf bound_ctrl:1
	ds_read_b32 v206, v198 offset:38912
	v_pk_fma_f32 v[214:215], v[218:219], v[228:229], v[214:215] op_sel_hi:[0,1,1]
	v_pk_fma_f32 v[216:217], v[218:219], v[230:231], v[216:217] op_sel_hi:[0,1,1]
	v_cndmask_b32_e64 v242, v242, v240, s[22:23]
	v_pk_fma_f32 v[156:157], v[156:157], v[220:221], v[214:215]
	v_pk_fma_f32 v[158:159], v[158:159], v[222:223], v[216:217]
	ds_read_b128 v[118:121], v197 offset:37664
	ds_read_b128 v[110:113], v197 offset:37632
	ds_read_b128 v[126:129], v197 offset:37696
	s_waitcnt lgkmcnt(6)
	v_pk_mul_f32 v[210:211], v[156:157], v[94:95]
	v_pk_mul_f32 v[212:213], v[236:237], v[156:157]
	v_pk_fma_f32 v[210:211], v[158:159], v[96:97], v[210:211]
	v_pk_fma_f32 v[212:213], v[158:159], v[238:239], v[212:213]
	v_add_f32_e32 v210, v210, v211
	v_add_f32_e32 v212, v212, v213
	v_pk_mul_f32 v[214:215], v[102:103], v[204:205] op_sel_hi:[1,0]
	v_add_f32_dpp v210, v210, v210 quad_perm:[1,0,3,2] row_mask:0xf bank_mask:0xf bound_ctrl:1
	v_add_f32_dpp v212, v212, v212 quad_perm:[1,0,3,2] row_mask:0xf bank_mask:0xf bound_ctrl:1
	v_pk_mul_f32 v[216:217], v[104:105], v[204:205] op_sel_hi:[1,0]
	v_add_f32_dpp v210, v210, v210 quad_perm:[2,3,0,1] row_mask:0xf bank_mask:0xf bound_ctrl:1
	v_add_f32_dpp v212, v212, v212 quad_perm:[2,3,0,1] row_mask:0xf bank_mask:0xf bound_ctrl:1
	ds_read_b128 v[224:227], v197 offset:38992
	v_add_f32_dpp v210, v210, v210 row_half_mirror row_mask:0xf bank_mask:0xf bound_ctrl:1
	v_add_f32_dpp v212, v212, v212 row_half_mirror row_mask:0xf bank_mask:0xf bound_ctrl:1
	ds_read_b128 v[232:235], v197 offset:39024
	v_add_f32_dpp v218, v210, v210 row_mirror row_mask:0xf bank_mask:0xf bound_ctrl:1
	v_add_f32_dpp v240, v212, v212 row_mirror row_mask:0xf bank_mask:0xf bound_ctrl:1
	ds_read_b32 v208, v198 offset:40256
	v_pk_fma_f32 v[214:215], v[218:219], v[98:99], v[214:215] op_sel_hi:[0,1,1]
	v_pk_fma_f32 v[216:217], v[218:219], v[100:101], v[216:217] op_sel_hi:[0,1,1]
	v_cndmask_b32_e64 v242, v242, v240, s[24:25]
	v_pk_fma_f32 v[156:157], v[156:157], v[90:91], v[214:215]
	v_pk_fma_f32 v[158:159], v[158:159], v[92:93], v[216:217]
	ds_read_b128 v[228:231], v197 offset:39008
	ds_read_b128 v[220:223], v197 offset:38976
	ds_read_b128 v[236:239], v197 offset:39040
	s_waitcnt lgkmcnt(6)
	v_pk_mul_f32 v[210:211], v[156:157], v[114:115]
	v_pk_mul_f32 v[212:213], v[106:107], v[156:157]
	v_pk_fma_f32 v[210:211], v[158:159], v[116:117], v[210:211]
	v_pk_fma_f32 v[212:213], v[158:159], v[108:109], v[212:213]
	v_add_f32_e32 v210, v210, v211
	v_add_f32_e32 v212, v212, v213
	v_pk_mul_f32 v[214:215], v[122:123], v[206:207] op_sel_hi:[1,0]
	v_add_f32_dpp v210, v210, v210 quad_perm:[1,0,3,2] row_mask:0xf bank_mask:0xf bound_ctrl:1
	v_add_f32_dpp v212, v212, v212 quad_perm:[1,0,3,2] row_mask:0xf bank_mask:0xf bound_ctrl:1
	v_pk_mul_f32 v[216:217], v[124:125], v[206:207] op_sel_hi:[1,0]
	v_add_f32_dpp v210, v210, v210 quad_perm:[2,3,0,1] row_mask:0xf bank_mask:0xf bound_ctrl:1
	v_add_f32_dpp v212, v212, v212 quad_perm:[2,3,0,1] row_mask:0xf bank_mask:0xf bound_ctrl:1
	ds_read_b128 v[94:97], v197 offset:40336
	v_add_f32_dpp v210, v210, v210 row_half_mirror row_mask:0xf bank_mask:0xf bound_ctrl:1
	v_add_f32_dpp v212, v212, v212 row_half_mirror row_mask:0xf bank_mask:0xf bound_ctrl:1
	ds_read_b128 v[102:105], v197 offset:40368
	v_add_f32_dpp v218, v210, v210 row_mirror row_mask:0xf bank_mask:0xf bound_ctrl:1
	v_add_f32_dpp v240, v212, v212 row_mirror row_mask:0xf bank_mask:0xf bound_ctrl:1
	ds_read_b32 v204, v198 offset:41600
	v_pk_fma_f32 v[214:215], v[218:219], v[118:119], v[214:215] op_sel_hi:[0,1,1]
	v_pk_fma_f32 v[216:217], v[218:219], v[120:121], v[216:217] op_sel_hi:[0,1,1]
	v_cndmask_b32_e64 v242, v242, v240, s[26:27]
	v_pk_fma_f32 v[156:157], v[156:157], v[110:111], v[214:215]
	v_pk_fma_f32 v[158:159], v[158:159], v[112:113], v[216:217]
	ds_read_b128 v[98:101], v197 offset:40352
	ds_read_b128 v[90:93], v197 offset:40320
	ds_read_b128 v[106:109], v197 offset:40384
	s_waitcnt lgkmcnt(6)
	v_pk_mul_f32 v[210:211], v[156:157], v[224:225]
	v_pk_mul_f32 v[212:213], v[126:127], v[156:157]
	v_pk_fma_f32 v[210:211], v[158:159], v[226:227], v[210:211]
	v_pk_fma_f32 v[212:213], v[158:159], v[128:129], v[212:213]
	v_add_f32_e32 v210, v210, v211
	v_add_f32_e32 v212, v212, v213
	v_pk_mul_f32 v[214:215], v[232:233], v[208:209] op_sel_hi:[1,0]
	v_add_f32_dpp v210, v210, v210 quad_perm:[1,0,3,2] row_mask:0xf bank_mask:0xf bound_ctrl:1
	v_add_f32_dpp v212, v212, v212 quad_perm:[1,0,3,2] row_mask:0xf bank_mask:0xf bound_ctrl:1
	v_pk_mul_f32 v[216:217], v[234:235], v[208:209] op_sel_hi:[1,0]
	v_add_f32_dpp v210, v210, v210 quad_perm:[2,3,0,1] row_mask:0xf bank_mask:0xf bound_ctrl:1
	v_add_f32_dpp v212, v212, v212 quad_perm:[2,3,0,1] row_mask:0xf bank_mask:0xf bound_ctrl:1
	ds_read_b128 v[114:117], v197 offset:41680
	v_add_f32_dpp v210, v210, v210 row_half_mirror row_mask:0xf bank_mask:0xf bound_ctrl:1
	v_add_f32_dpp v212, v212, v212 row_half_mirror row_mask:0xf bank_mask:0xf bound_ctrl:1
	ds_read_b128 v[122:125], v197 offset:41712
	v_add_f32_dpp v218, v210, v210 row_mirror row_mask:0xf bank_mask:0xf bound_ctrl:1
	v_add_f32_dpp v240, v212, v212 row_mirror row_mask:0xf bank_mask:0xf bound_ctrl:1
	ds_read_b32 v206, v198 offset:42944
	v_pk_fma_f32 v[214:215], v[218:219], v[228:229], v[214:215] op_sel_hi:[0,1,1]
	v_pk_fma_f32 v[216:217], v[218:219], v[230:231], v[216:217] op_sel_hi:[0,1,1]
	v_cndmask_b32_e64 v242, v242, v240, s[28:29]
	v_pk_fma_f32 v[156:157], v[156:157], v[220:221], v[214:215]
	v_pk_fma_f32 v[158:159], v[158:159], v[222:223], v[216:217]
	ds_read_b128 v[118:121], v197 offset:41696
	ds_read_b128 v[110:113], v197 offset:41664
	ds_read_b128 v[126:129], v197 offset:41728
	s_waitcnt lgkmcnt(6)
	v_pk_mul_f32 v[210:211], v[156:157], v[94:95]
	v_pk_mul_f32 v[212:213], v[236:237], v[156:157]
	v_pk_fma_f32 v[210:211], v[158:159], v[96:97], v[210:211]
	v_pk_fma_f32 v[212:213], v[158:159], v[238:239], v[212:213]
	v_add_f32_e32 v210, v210, v211
	v_add_f32_e32 v212, v212, v213
	v_pk_mul_f32 v[214:215], v[102:103], v[204:205] op_sel_hi:[1,0]
	v_add_f32_dpp v210, v210, v210 quad_perm:[1,0,3,2] row_mask:0xf bank_mask:0xf bound_ctrl:1
	v_add_f32_dpp v212, v212, v212 quad_perm:[1,0,3,2] row_mask:0xf bank_mask:0xf bound_ctrl:1
	v_pk_mul_f32 v[216:217], v[104:105], v[204:205] op_sel_hi:[1,0]
	v_add_f32_dpp v210, v210, v210 quad_perm:[2,3,0,1] row_mask:0xf bank_mask:0xf bound_ctrl:1
	v_add_f32_dpp v212, v212, v212 quad_perm:[2,3,0,1] row_mask:0xf bank_mask:0xf bound_ctrl:1
	s_nop 0
	v_add_f32_dpp v210, v210, v210 row_half_mirror row_mask:0xf bank_mask:0xf bound_ctrl:1
	v_add_f32_dpp v212, v212, v212 row_half_mirror row_mask:0xf bank_mask:0xf bound_ctrl:1
	s_nop 0
	v_add_f32_dpp v218, v210, v210 row_mirror row_mask:0xf bank_mask:0xf bound_ctrl:1
	v_add_f32_dpp v240, v212, v212 row_mirror row_mask:0xf bank_mask:0xf bound_ctrl:1
	s_nop 0
	v_pk_fma_f32 v[214:215], v[218:219], v[98:99], v[214:215] op_sel_hi:[0,1,1]
	v_pk_fma_f32 v[216:217], v[218:219], v[100:101], v[216:217] op_sel_hi:[0,1,1]
	v_cndmask_b32_e64 v242, v242, v240, s[30:31]
	v_pk_fma_f32 v[156:157], v[156:157], v[90:91], v[214:215]
	v_pk_fma_f32 v[158:159], v[158:159], v[92:93], v[216:217]
	s_nop 0
	s_nop 0
	s_nop 0
	s_waitcnt lgkmcnt(0)
	v_pk_mul_f32 v[210:211], v[156:157], v[114:115]
	v_pk_mul_f32 v[212:213], v[106:107], v[156:157]
	v_pk_fma_f32 v[210:211], v[158:159], v[116:117], v[210:211]
	v_pk_fma_f32 v[212:213], v[158:159], v[108:109], v[212:213]
	v_add_f32_e32 v210, v210, v211
	v_add_f32_e32 v212, v212, v213
	v_pk_mul_f32 v[214:215], v[122:123], v[206:207] op_sel_hi:[1,0]
	v_add_f32_dpp v210, v210, v210 quad_perm:[1,0,3,2] row_mask:0xf bank_mask:0xf bound_ctrl:1
	v_add_f32_dpp v212, v212, v212 quad_perm:[1,0,3,2] row_mask:0xf bank_mask:0xf bound_ctrl:1
	v_pk_mul_f32 v[216:217], v[124:125], v[206:207] op_sel_hi:[1,0]
	v_add_f32_dpp v210, v210, v210 quad_perm:[2,3,0,1] row_mask:0xf bank_mask:0xf bound_ctrl:1
	v_add_f32_dpp v212, v212, v212 quad_perm:[2,3,0,1] row_mask:0xf bank_mask:0xf bound_ctrl:1
	s_nop 0
	v_add_f32_dpp v210, v210, v210 row_half_mirror row_mask:0xf bank_mask:0xf bound_ctrl:1
	v_add_f32_dpp v212, v212, v212 row_half_mirror row_mask:0xf bank_mask:0xf bound_ctrl:1
	s_nop 0
	v_add_f32_dpp v218, v210, v210 row_mirror row_mask:0xf bank_mask:0xf bound_ctrl:1
	v_add_f32_dpp v240, v212, v212 row_mirror row_mask:0xf bank_mask:0xf bound_ctrl:1
	s_nop 0
	v_pk_fma_f32 v[214:215], v[218:219], v[118:119], v[214:215] op_sel_hi:[0,1,1]
	v_pk_fma_f32 v[216:217], v[218:219], v[120:121], v[216:217] op_sel_hi:[0,1,1]
	v_cndmask_b32_e64 v242, v242, v240, s[34:35]
	v_pk_fma_f32 v[156:157], v[156:157], v[110:111], v[214:215]
	v_pk_fma_f32 v[158:159], v[158:159], v[112:113], v[216:217]
	s_nop 0
	s_nop 0
	s_nop 0
	s_nop 0
	v_pk_mul_f32 v[212:213], v[126:127], v[156:157]
	s_nop 0
	v_pk_fma_f32 v[212:213], v[158:159], v[128:129], v[212:213]
	s_nop 0
	v_add_f32_e32 v212, v212, v213
	s_nop 0
	s_nop 0
	v_add_f32_dpp v212, v212, v212 quad_perm:[1,0,3,2] row_mask:0xf bank_mask:0xf bound_ctrl:1
	s_nop 0
	s_nop 0
	v_add_f32_dpp v212, v212, v212 quad_perm:[2,3,0,1] row_mask:0xf bank_mask:0xf bound_ctrl:1
	s_nop 0
	s_nop 0
	v_add_f32_dpp v212, v212, v212 row_half_mirror row_mask:0xf bank_mask:0xf bound_ctrl:1
	s_nop 0
	s_nop 0
	v_add_f32_dpp v240, v212, v212 row_mirror row_mask:0xf bank_mask:0xf bound_ctrl:1
	s_nop 0
	s_nop 0
	s_nop 0
	v_cndmask_b32_e64 v242, v242, v240, s[36:37]
	v_or_b32_e32 v100, s56, v137
	v_xad_u32 v101, v100, -1, s57
	v_or_b32_e32 v103, 16, v100
	v_cndmask_b32_e64 v100, v101, v100, s[38:39]
	v_bitop3_b32 v102, s56, v202, v137 bitop3:0x36
	v_add_u32_e32 v102, s57, v102
	v_cndmask_b32_e64 v102, v102, v103, s[38:39]
	v_add_u32_e32 v100, s58, v100
	v_add_u32_e32 v102, s58, v102
	v_ashrrev_i32_e32 v101, 31, v100
	v_ashrrev_i32_e32 v103, 31, v102
	v_lshlrev_b64 v[100:101], 12, v[100:101]
	v_lshlrev_b64 v[102:103], 12, v[102:103]
	v_lshl_add_u64 v[100:101], v[148:149], 0, v[100:101]
	v_lshl_add_u64 v[102:103], v[148:149], 0, v[102:103]
	global_store_dword v[100:101], v241, off
	global_store_dword v[102:103], v242, off
	v_mov_b64_e32 v[90:91], v[156:157]
	v_mov_b64_e32 v[92:93], v[158:159]
	s_setprio 0
	s_mov_b64 s[56:57], 0

.LBB0_685:
	s_waitcnt lgkmcnt(0)
	s_barrier
	s_mov_b64 s[56:57], -1
	s_and_b64 vcc, exec, s[0:1]
	s_cbranch_vccz .LBB0_687
	s_setprio 3
	s_add_i32 s56, s2, 0xffffff00
	s_cmp_lt_u32 s79, 8
	s_cselect_b32 s56, s2, s56
	s_cselect_b32 s58, s81, 0x1000
	s_cselect_b32 s57, s3, s78
	ds_read_b128 v[94:97], v200 offset:16
	ds_read_b128 v[102:105], v200 offset:48
	ds_read_b32 v204, v201
	ds_read_b128 v[98:101], v200 offset:32
	ds_read_b128 v[90:93], v200
	ds_read_b128 v[106:109], v200 offset:64
	ds_read_b128 v[114:117], v200 offset:1360
	ds_read_b128 v[122:125], v200 offset:1392
	ds_read_b32 v206, v201 offset:1344
	ds_read_b128 v[118:121], v200 offset:1376
	ds_read_b128 v[110:113], v200 offset:1344
	ds_read_b128 v[126:129], v200 offset:1408
	s_waitcnt lgkmcnt(6)
	v_pk_mul_f32 v[210:211], v[156:157], v[94:95]
	s_nop 0
	v_pk_fma_f32 v[210:211], v[158:159], v[96:97], v[210:211]
	s_nop 0
	v_add_f32_e32 v210, v210, v211
	s_nop 0
	v_pk_mul_f32 v[214:215], v[102:103], v[204:205] op_sel_hi:[1,0]
	v_add_f32_dpp v210, v210, v210 quad_perm:[1,0,3,2] row_mask:0xf bank_mask:0xf bound_ctrl:1
	s_nop 0
	v_pk_mul_f32 v[216:217], v[104:105], v[204:205] op_sel_hi:[1,0]
	v_add_f32_dpp v210, v210, v210 quad_perm:[2,3,0,1] row_mask:0xf bank_mask:0xf bound_ctrl:1
	s_nop 0
	ds_read_b128 v[224:227], v200 offset:2704
	v_add_f32_dpp v210, v210, v210 row_half_mirror row_mask:0xf bank_mask:0xf bound_ctrl:1
	s_nop 0
	ds_read_b128 v[232:235], v200 offset:2736
	v_add_f32_dpp v218, v210, v210 row_mirror row_mask:0xf bank_mask:0xf bound_ctrl:1
	s_nop 0
	ds_read_b32 v208, v201 offset:2688
	v_pk_fma_f32 v[214:215], v[218:219], v[98:99], v[214:215] op_sel_hi:[0,1,1]
	v_pk_fma_f32 v[216:217], v[218:219], v[100:101], v[216:217] op_sel_hi:[0,1,1]
	s_nop 0
	v_pk_fma_f32 v[156:157], v[156:157], v[90:91], v[214:215]
	v_pk_fma_f32 v[158:159], v[158:159], v[92:93], v[216:217]
	ds_read_b128 v[228:231], v200 offset:2720
	ds_read_b128 v[220:223], v200 offset:2688
	ds_read_b128 v[236:239], v200 offset:2752
	s_waitcnt lgkmcnt(6)
	v_pk_mul_f32 v[210:211], v[156:157], v[114:115]
	v_pk_mul_f32 v[212:213], v[106:107], v[156:157]
	v_pk_fma_f32 v[210:211], v[158:159], v[116:117], v[210:211]
	v_pk_fma_f32 v[212:213], v[158:159], v[108:109], v[212:213]
	v_add_f32_e32 v210, v210, v211
	v_add_f32_e32 v212, v212, v213
	v_pk_mul_f32 v[214:215], v[122:123], v[206:207] op_sel_hi:[1,0]
	v_add_f32_dpp v210, v210, v210 quad_perm:[1,0,3,2] row_mask:0xf bank_mask:0xf bound_ctrl:1
	v_add_f32_dpp v212, v212, v212 quad_perm:[1,0,3,2] row_mask:0xf bank_mask:0xf bound_ctrl:1
	v_pk_mul_f32 v[216:217], v[124:125], v[206:207] op_sel_hi:[1,0]
	v_add_f32_dpp v210, v210, v210 quad_perm:[2,3,0,1] row_mask:0xf bank_mask:0xf bound_ctrl:1
	v_add_f32_dpp v212, v212, v212 quad_perm:[2,3,0,1] row_mask:0xf bank_mask:0xf bound_ctrl:1
	ds_read_b128 v[94:97], v200 offset:4048
	v_add_f32_dpp v210, v210, v210 row_half_mirror row_mask:0xf bank_mask:0xf bound_ctrl:1
	v_add_f32_dpp v212, v212, v212 row_half_mirror row_mask:0xf bank_mask:0xf bound_ctrl:1
	ds_read_b128 v[102:105], v200 offset:4080
	v_add_f32_dpp v218, v210, v210 row_mirror row_mask:0xf bank_mask:0xf bound_ctrl:1
	v_add_f32_dpp v240, v212, v212 row_mirror row_mask:0xf bank_mask:0xf bound_ctrl:1
	ds_read_b32 v204, v201 offset:4032
	v_pk_fma_f32 v[214:215], v[218:219], v[118:119], v[214:215] op_sel_hi:[0,1,1]
	v_pk_fma_f32 v[216:217], v[218:219], v[120:121], v[216:217] op_sel_hi:[0,1,1]
	v_cndmask_b32_e64 v241, 0, v240, s[4:5]
	v_pk_fma_f32 v[156:157], v[156:157], v[110:111], v[214:215]
	v_pk_fma_f32 v[158:159], v[158:159], v[112:113], v[216:217]
	ds_read_b128 v[98:101], v200 offset:4064
	ds_read_b128 v[90:93], v200 offset:4032
	ds_read_b128 v[106:109], v200 offset:4096
	s_waitcnt lgkmcnt(6)
	v_pk_mul_f32 v[210:211], v[156:157], v[224:225]
	v_pk_mul_f32 v[212:213], v[126:127], v[156:157]
	v_pk_fma_f32 v[210:211], v[158:159], v[226:227], v[210:211]
	v_pk_fma_f32 v[212:213], v[158:159], v[128:129], v[212:213]
	v_add_f32_e32 v210, v210, v211
	v_add_f32_e32 v212, v212, v213
	v_pk_mul_f32 v[214:215], v[232:233], v[208:209] op_sel_hi:[1,0]
	v_add_f32_dpp v210, v210, v210 quad_perm:[1,0,3,2] row_mask:0xf bank_mask:0xf bound_ctrl:1
	v_add_f32_dpp v212, v212, v212 quad_perm:[1,0,3,2] row_mask:0xf bank_mask:0xf bound_ctrl:1
	v_pk_mul_f32 v[216:217], v[234:235], v[208:209] op_sel_hi:[1,0]
	v_add_f32_dpp v210, v210, v210 quad_perm:[2,3,0,1] row_mask:0xf bank_mask:0xf bound_ctrl:1
	v_add_f32_dpp v212, v212, v212 quad_perm:[2,3,0,1] row_mask:0xf bank_mask:0xf bound_ctrl:1
	ds_read_b128 v[114:117], v200 offset:5392
	v_add_f32_dpp v210, v210, v210 row_half_mirror row_mask:0xf bank_mask:0xf bound_ctrl:1
	v_add_f32_dpp v212, v212, v212 row_half_mirror row_mask:0xf bank_mask:0xf bound_ctrl:1
	ds_read_b128 v[122:125], v200 offset:5424
	v_add_f32_dpp v218, v210, v210 row_mirror row_mask:0xf bank_mask:0xf bound_ctrl:1
	v_add_f32_dpp v240, v212, v212 row_mirror row_mask:0xf bank_mask:0xf bound_ctrl:1
	ds_read_b32 v206, v201 offset:5376
	v_pk_fma_f32 v[214:215], v[218:219], v[228:229], v[214:215] op_sel_hi:[0,1,1]
	v_pk_fma_f32 v[216:217], v[218:219], v[230:231], v[216:217] op_sel_hi:[0,1,1]
	v_cndmask_b32_e64 v241, v241, v240, s[6:7]
	v_pk_fma_f32 v[156:157], v[156:157], v[220:221], v[214:215]
	v_pk_fma_f32 v[158:159], v[158:159], v[222:223], v[216:217]
	ds_read_b128 v[118:121], v200 offset:5408
	ds_read_b128 v[110:113], v200 offset:5376
	ds_read_b128 v[126:129], v200 offset:5440
	s_waitcnt lgkmcnt(6)
	v_pk_mul_f32 v[210:211], v[156:157], v[94:95]
	v_pk_mul_f32 v[212:213], v[236:237], v[156:157]
	v_pk_fma_f32 v[210:211], v[158:159], v[96:97], v[210:211]
	v_pk_fma_f32 v[212:213], v[158:159], v[238:239], v[212:213]
	v_add_f32_e32 v210, v210, v211
	v_add_f32_e32 v212, v212, v213
	v_pk_mul_f32 v[214:215], v[102:103], v[204:205] op_sel_hi:[1,0]
	v_add_f32_dpp v210, v210, v210 quad_perm:[1,0,3,2] row_mask:0xf bank_mask:0xf bound_ctrl:1
	v_add_f32_dpp v212, v212, v212 quad_perm:[1,0,3,2] row_mask:0xf bank_mask:0xf bound_ctrl:1
	v_pk_mul_f32 v[216:217], v[104:105], v[204:205] op_sel_hi:[1,0]
	v_add_f32_dpp v210, v210, v210 quad_perm:[2,3,0,1] row_mask:0xf bank_mask:0xf bound_ctrl:1
	v_add_f32_dpp v212, v212, v212 quad_perm:[2,3,0,1] row_mask:0xf bank_mask:0xf bound_ctrl:1
	ds_read_b128 v[224:227], v200 offset:6736
	v_add_f32_dpp v210, v210, v210 row_half_mirror row_mask:0xf bank_mask:0xf bound_ctrl:1
	v_add_f32_dpp v212, v212, v212 row_half_mirror row_mask:0xf bank_mask:0xf bound_ctrl:1
	ds_read_b128 v[232:235], v200 offset:6768
	v_add_f32_dpp v218, v210, v210 row_mirror row_mask:0xf bank_mask:0xf bound_ctrl:1
	v_add_f32_dpp v240, v212, v212 row_mirror row_mask:0xf bank_mask:0xf bound_ctrl:1
	ds_read_b32 v208, v201 offset:6720
	v_pk_fma_f32 v[214:215], v[218:219], v[98:99], v[214:215] op_sel_hi:[0,1,1]
	v_pk_fma_f32 v[216:217], v[218:219], v[100:101], v[216:217] op_sel_hi:[0,1,1]
	v_cndmask_b32_e64 v241, v241, v240, s[8:9]
	v_pk_fma_f32 v[156:157], v[156:157], v[90:91], v[214:215]
	v_pk_fma_f32 v[158:159], v[158:159], v[92:93], v[216:217]
	ds_read_b128 v[228:231], v200 offset:6752
	ds_read_b128 v[220:223], v200 offset:6720
	ds_read_b128 v[236:239], v200 offset:6784
	s_waitcnt lgkmcnt(6)
	v_pk_mul_f32 v[210:211], v[156:157], v[114:115]
	v_pk_mul_f32 v[212:213], v[106:107], v[156:157]
	v_pk_fma_f32 v[210:211], v[158:159], v[116:117], v[210:211]
	v_pk_fma_f32 v[212:213], v[158:159], v[108:109], v[212:213]
	v_add_f32_e32 v210, v210, v211
	v_add_f32_e32 v212, v212, v213
	v_pk_mul_f32 v[214:215], v[122:123], v[206:207] op_sel_hi:[1,0]
	v_add_f32_dpp v210, v210, v210 quad_perm:[1,0,3,2] row_mask:0xf bank_mask:0xf bound_ctrl:1
	v_add_f32_dpp v212, v212, v212 quad_perm:[1,0,3,2] row_mask:0xf bank_mask:0xf bound_ctrl:1
	v_pk_mul_f32 v[216:217], v[124:125], v[206:207] op_sel_hi:[1,0]
	v_add_f32_dpp v210, v210, v210 quad_perm:[2,3,0,1] row_mask:0xf bank_mask:0xf bound_ctrl:1
	v_add_f32_dpp v212, v212, v212 quad_perm:[2,3,0,1] row_mask:0xf bank_mask:0xf bound_ctrl:1
	ds_read_b128 v[94:97], v200 offset:8080
	v_add_f32_dpp v210, v210, v210 row_half_mirror row_mask:0xf bank_mask:0xf bound_ctrl:1
	v_add_f32_dpp v212, v212, v212 row_half_mirror row_mask:0xf bank_mask:0xf bound_ctrl:1
	ds_read_b128 v[102:105], v200 offset:8112
	v_add_f32_dpp v218, v210, v210 row_mirror row_mask:0xf bank_mask:0xf bound_ctrl:1
	v_add_f32_dpp v240, v212, v212 row_mirror row_mask:0xf bank_mask:0xf bound_ctrl:1
	ds_read_b32 v204, v201 offset:8064
	v_pk_fma_f32 v[214:215], v[218:219], v[118:119], v[214:215] op_sel_hi:[0,1,1]
	v_pk_fma_f32 v[216:217], v[218:219], v[120:121], v[216:217] op_sel_hi:[0,1,1]
	v_cndmask_b32_e64 v241, v241, v240, s[10:11]
	v_pk_fma_f32 v[156:157], v[156:157], v[110:111], v[214:215]
	v_pk_fma_f32 v[158:159], v[158:159], v[112:113], v[216:217]
	ds_read_b128 v[98:101], v200 offset:8096
	ds_read_b128 v[90:93], v200 offset:8064
	ds_read_b128 v[106:109], v200 offset:8128
	s_waitcnt lgkmcnt(6)
	v_pk_mul_f32 v[210:211], v[156:157], v[224:225]
	v_pk_mul_f32 v[212:213], v[126:127], v[156:157]
	v_pk_fma_f32 v[210:211], v[158:159], v[226:227], v[210:211]
	v_pk_fma_f32 v[212:213], v[158:159], v[128:129], v[212:213]
	v_add_f32_e32 v210, v210, v211
	v_add_f32_e32 v212, v212, v213
	v_pk_mul_f32 v[214:215], v[232:233], v[208:209] op_sel_hi:[1,0]
	v_add_f32_dpp v210, v210, v210 quad_perm:[1,0,3,2] row_mask:0xf bank_mask:0xf bound_ctrl:1
	v_add_f32_dpp v212, v212, v212 quad_perm:[1,0,3,2] row_mask:0xf bank_mask:0xf bound_ctrl:1
	v_pk_mul_f32 v[216:217], v[234:235], v[208:209] op_sel_hi:[1,0]
	v_add_f32_dpp v210, v210, v210 quad_perm:[2,3,0,1] row_mask:0xf bank_mask:0xf bound_ctrl:1
	v_add_f32_dpp v212, v212, v212 quad_perm:[2,3,0,1] row_mask:0xf bank_mask:0xf bound_ctrl:1
	ds_read_b128 v[114:117], v200 offset:9424
	v_add_f32_dpp v210, v210, v210 row_half_mirror row_mask:0xf bank_mask:0xf bound_ctrl:1
	v_add_f32_dpp v212, v212, v212 row_half_mirror row_mask:0xf bank_mask:0xf bound_ctrl:1
	ds_read_b128 v[122:125], v200 offset:9456
	v_add_f32_dpp v218, v210, v210 row_mirror row_mask:0xf bank_mask:0xf bound_ctrl:1
	v_add_f32_dpp v240, v212, v212 row_mirror row_mask:0xf bank_mask:0xf bound_ctrl:1
	ds_read_b32 v206, v201 offset:9408
	v_pk_fma_f32 v[214:215], v[218:219], v[228:229], v[214:215] op_sel_hi:[0,1,1]
	v_pk_fma_f32 v[216:217], v[218:219], v[230:231], v[216:217] op_sel_hi:[0,1,1]
	v_cndmask_b32_e64 v241, v241, v240, s[12:13]
	v_pk_fma_f32 v[156:157], v[156:157], v[220:221], v[214:215]
	v_pk_fma_f32 v[158:159], v[158:159], v[222:223], v[216:217]
	ds_read_b128 v[118:121], v200 offset:9440
	ds_read_b128 v[110:113], v200 offset:9408
	ds_read_b128 v[126:129], v200 offset:9472
	s_waitcnt lgkmcnt(6)
	v_pk_mul_f32 v[210:211], v[156:157], v[94:95]
	v_pk_mul_f32 v[212:213], v[236:237], v[156:157]
	v_pk_fma_f32 v[210:211], v[158:159], v[96:97], v[210:211]
	v_pk_fma_f32 v[212:213], v[158:159], v[238:239], v[212:213]
	v_add_f32_e32 v210, v210, v211
	v_add_f32_e32 v212, v212, v213
	v_pk_mul_f32 v[214:215], v[102:103], v[204:205] op_sel_hi:[1,0]
	v_add_f32_dpp v210, v210, v210 quad_perm:[1,0,3,2] row_mask:0xf bank_mask:0xf bound_ctrl:1
	v_add_f32_dpp v212, v212, v212 quad_perm:[1,0,3,2] row_mask:0xf bank_mask:0xf bound_ctrl:1
	v_pk_mul_f32 v[216:217], v[104:105], v[204:205] op_sel_hi:[1,0]
	v_add_f32_dpp v210, v210, v210 quad_perm:[2,3,0,1] row_mask:0xf bank_mask:0xf bound_ctrl:1
	v_add_f32_dpp v212, v212, v212 quad_perm:[2,3,0,1] row_mask:0xf bank_mask:0xf bound_ctrl:1
	ds_read_b128 v[224:227], v200 offset:10768
	v_add_f32_dpp v210, v210, v210 row_half_mirror row_mask:0xf bank_mask:0xf bound_ctrl:1
	v_add_f32_dpp v212, v212, v212 row_half_mirror row_mask:0xf bank_mask:0xf bound_ctrl:1
	ds_read_b128 v[232:235], v200 offset:10800
	v_add_f32_dpp v218, v210, v210 row_mirror row_mask:0xf bank_mask:0xf bound_ctrl:1
	v_add_f32_dpp v240, v212, v212 row_mirror row_mask:0xf bank_mask:0xf bound_ctrl:1
	ds_read_b32 v208, v201 offset:10752
	v_pk_fma_f32 v[214:215], v[218:219], v[98:99], v[214:215] op_sel_hi:[0,1,1]
	v_pk_fma_f32 v[216:217], v[218:219], v[100:101], v[216:217] op_sel_hi:[0,1,1]
	v_cndmask_b32_e64 v241, v241, v240, s[14:15]
	v_pk_fma_f32 v[156:157], v[156:157], v[90:91], v[214:215]
	v_pk_fma_f32 v[158:159], v[158:159], v[92:93], v[216:217]
	ds_read_b128 v[228:231], v200 offset:10784
	ds_read_b128 v[220:223], v200 offset:10752
	ds_read_b128 v[236:239], v200 offset:10816
	s_waitcnt lgkmcnt(6)
	v_pk_mul_f32 v[210:211], v[156:157], v[114:115]
	v_pk_mul_f32 v[212:213], v[106:107], v[156:157]
	v_pk_fma_f32 v[210:211], v[158:159], v[116:117], v[210:211]
	v_pk_fma_f32 v[212:213], v[158:159], v[108:109], v[212:213]
	v_add_f32_e32 v210, v210, v211
	v_add_f32_e32 v212, v212, v213
	v_pk_mul_f32 v[214:215], v[122:123], v[206:207] op_sel_hi:[1,0]
	v_add_f32_dpp v210, v210, v210 quad_perm:[1,0,3,2] row_mask:0xf bank_mask:0xf bound_ctrl:1
	v_add_f32_dpp v212, v212, v212 quad_perm:[1,0,3,2] row_mask:0xf bank_mask:0xf bound_ctrl:1
	v_pk_mul_f32 v[216:217], v[124:125], v[206:207] op_sel_hi:[1,0]
	v_add_f32_dpp v210, v210, v210 quad_perm:[2,3,0,1] row_mask:0xf bank_mask:0xf bound_ctrl:1
	v_add_f32_dpp v212, v212, v212 quad_perm:[2,3,0,1] row_mask:0xf bank_mask:0xf bound_ctrl:1
	ds_read_b128 v[94:97], v200 offset:12112
	v_add_f32_dpp v210, v210, v210 row_half_mirror row_mask:0xf bank_mask:0xf bound_ctrl:1
	v_add_f32_dpp v212, v212, v212 row_half_mirror row_mask:0xf bank_mask:0xf bound_ctrl:1
	ds_read_b128 v[102:105], v200 offset:12144
	v_add_f32_dpp v218, v210, v210 row_mirror row_mask:0xf bank_mask:0xf bound_ctrl:1
	v_add_f32_dpp v240, v212, v212 row_mirror row_mask:0xf bank_mask:0xf bound_ctrl:1
	ds_read_b32 v204, v201 offset:12096
	v_pk_fma_f32 v[214:215], v[218:219], v[118:119], v[214:215] op_sel_hi:[0,1,1]
	v_pk_fma_f32 v[216:217], v[218:219], v[120:121], v[216:217] op_sel_hi:[0,1,1]
	v_cndmask_b32_e64 v241, v241, v240, s[16:17]
	v_pk_fma_f32 v[156:157], v[156:157], v[110:111], v[214:215]
	v_pk_fma_f32 v[158:159], v[158:159], v[112:113], v[216:217]
	ds_read_b128 v[98:101], v200 offset:12128
	ds_read_b128 v[90:93], v200 offset:12096
	ds_read_b128 v[106:109], v200 offset:12160
	s_waitcnt lgkmcnt(6)
	v_pk_mul_f32 v[210:211], v[156:157], v[224:225]
	v_pk_mul_f32 v[212:213], v[126:127], v[156:157]
	v_pk_fma_f32 v[210:211], v[158:159], v[226:227], v[210:211]
	v_pk_fma_f32 v[212:213], v[158:159], v[128:129], v[212:213]
	v_add_f32_e32 v210, v210, v211
	v_add_f32_e32 v212, v212, v213
	v_pk_mul_f32 v[214:215], v[232:233], v[208:209] op_sel_hi:[1,0]
	v_add_f32_dpp v210, v210, v210 quad_perm:[1,0,3,2] row_mask:0xf bank_mask:0xf bound_ctrl:1
	v_add_f32_dpp v212, v212, v212 quad_perm:[1,0,3,2] row_mask:0xf bank_mask:0xf bound_ctrl:1
	v_pk_mul_f32 v[216:217], v[234:235], v[208:209] op_sel_hi:[1,0]
	v_add_f32_dpp v210, v210, v210 quad_perm:[2,3,0,1] row_mask:0xf bank_mask:0xf bound_ctrl:1
	v_add_f32_dpp v212, v212, v212 quad_perm:[2,3,0,1] row_mask:0xf bank_mask:0xf bound_ctrl:1
	ds_read_b128 v[114:117], v200 offset:13456
	v_add_f32_dpp v210, v210, v210 row_half_mirror row_mask:0xf bank_mask:0xf bound_ctrl:1
	v_add_f32_dpp v212, v212, v212 row_half_mirror row_mask:0xf bank_mask:0xf bound_ctrl:1
	ds_read_b128 v[122:125], v200 offset:13488
	v_add_f32_dpp v218, v210, v210 row_mirror row_mask:0xf bank_mask:0xf bound_ctrl:1
	v_add_f32_dpp v240, v212, v212 row_mirror row_mask:0xf bank_mask:0xf bound_ctrl:1
	ds_read_b32 v206, v201 offset:13440
	v_pk_fma_f32 v[214:215], v[218:219], v[228:229], v[214:215] op_sel_hi:[0,1,1]
	v_pk_fma_f32 v[216:217], v[218:219], v[230:231], v[216:217] op_sel_hi:[0,1,1]
	v_cndmask_b32_e64 v241, v241, v240, s[18:19]
	v_pk_fma_f32 v[156:157], v[156:157], v[220:221], v[214:215]
	v_pk_fma_f32 v[158:159], v[158:159], v[222:223], v[216:217]
	ds_read_b128 v[118:121], v200 offset:13472
	ds_read_b128 v[110:113], v200 offset:13440
	ds_read_b128 v[126:129], v200 offset:13504
	s_waitcnt lgkmcnt(6)
	v_pk_mul_f32 v[210:211], v[156:157], v[94:95]
	v_pk_mul_f32 v[212:213], v[236:237], v[156:157]
	v_pk_fma_f32 v[210:211], v[158:159], v[96:97], v[210:211]
	v_pk_fma_f32 v[212:213], v[158:159], v[238:239], v[212:213]
	v_add_f32_e32 v210, v210, v211
	v_add_f32_e32 v212, v212, v213
	v_pk_mul_f32 v[214:215], v[102:103], v[204:205] op_sel_hi:[1,0]
	v_add_f32_dpp v210, v210, v210 quad_perm:[1,0,3,2] row_mask:0xf bank_mask:0xf bound_ctrl:1
	v_add_f32_dpp v212, v212, v212 quad_perm:[1,0,3,2] row_mask:0xf bank_mask:0xf bound_ctrl:1
	v_pk_mul_f32 v[216:217], v[104:105], v[204:205] op_sel_hi:[1,0]
	v_add_f32_dpp v210, v210, v210 quad_perm:[2,3,0,1] row_mask:0xf bank_mask:0xf bound_ctrl:1
	v_add_f32_dpp v212, v212, v212 quad_perm:[2,3,0,1] row_mask:0xf bank_mask:0xf bound_ctrl:1
	ds_read_b128 v[224:227], v200 offset:14800
	v_add_f32_dpp v210, v210, v210 row_half_mirror row_mask:0xf bank_mask:0xf bound_ctrl:1
	v_add_f32_dpp v212, v212, v212 row_half_mirror row_mask:0xf bank_mask:0xf bound_ctrl:1
	ds_read_b128 v[232:235], v200 offset:14832
	v_add_f32_dpp v218, v210, v210 row_mirror row_mask:0xf bank_mask:0xf bound_ctrl:1
	v_add_f32_dpp v240, v212, v212 row_mirror row_mask:0xf bank_mask:0xf bound_ctrl:1
	ds_read_b32 v208, v201 offset:14784
	v_pk_fma_f32 v[214:215], v[218:219], v[98:99], v[214:215] op_sel_hi:[0,1,1]
	v_pk_fma_f32 v[216:217], v[218:219], v[100:101], v[216:217] op_sel_hi:[0,1,1]
	v_cndmask_b32_e64 v241, v241, v240, s[20:21]
	v_pk_fma_f32 v[156:157], v[156:157], v[90:91], v[214:215]
	v_pk_fma_f32 v[158:159], v[158:159], v[92:93], v[216:217]
	ds_read_b128 v[228:231], v200 offset:14816
	ds_read_b128 v[220:223], v200 offset:14784
	ds_read_b128 v[236:239], v200 offset:14848
	s_waitcnt lgkmcnt(6)
	v_pk_mul_f32 v[210:211], v[156:157], v[114:115]
	v_pk_mul_f32 v[212:213], v[106:107], v[156:157]
	v_pk_fma_f32 v[210:211], v[158:159], v[116:117], v[210:211]
	v_pk_fma_f32 v[212:213], v[158:159], v[108:109], v[212:213]
	v_add_f32_e32 v210, v210, v211
	v_add_f32_e32 v212, v212, v213
	v_pk_mul_f32 v[214:215], v[122:123], v[206:207] op_sel_hi:[1,0]
	v_add_f32_dpp v210, v210, v210 quad_perm:[1,0,3,2] row_mask:0xf bank_mask:0xf bound_ctrl:1
	v_add_f32_dpp v212, v212, v212 quad_perm:[1,0,3,2] row_mask:0xf bank_mask:0xf bound_ctrl:1
	v_pk_mul_f32 v[216:217], v[124:125], v[206:207] op_sel_hi:[1,0]
	v_add_f32_dpp v210, v210, v210 quad_perm:[2,3,0,1] row_mask:0xf bank_mask:0xf bound_ctrl:1
	v_add_f32_dpp v212, v212, v212 quad_perm:[2,3,0,1] row_mask:0xf bank_mask:0xf bound_ctrl:1
	ds_read_b128 v[94:97], v200 offset:16144
	v_add_f32_dpp v210, v210, v210 row_half_mirror row_mask:0xf bank_mask:0xf bound_ctrl:1
	v_add_f32_dpp v212, v212, v212 row_half_mirror row_mask:0xf bank_mask:0xf bound_ctrl:1
	ds_read_b128 v[102:105], v200 offset:16176
	v_add_f32_dpp v218, v210, v210 row_mirror row_mask:0xf bank_mask:0xf bound_ctrl:1
	v_add_f32_dpp v240, v212, v212 row_mirror row_mask:0xf bank_mask:0xf bound_ctrl:1
	ds_read_b32 v204, v201 offset:16128
	v_pk_fma_f32 v[214:215], v[218:219], v[118:119], v[214:215] op_sel_hi:[0,1,1]
	v_pk_fma_f32 v[216:217], v[218:219], v[120:121], v[216:217] op_sel_hi:[0,1,1]
	v_cndmask_b32_e64 v241, v241, v240, s[22:23]
	v_pk_fma_f32 v[156:157], v[156:157], v[110:111], v[214:215]
	v_pk_fma_f32 v[158:159], v[158:159], v[112:113], v[216:217]
	ds_read_b128 v[98:101], v200 offset:16160
	ds_read_b128 v[90:93], v200 offset:16128
	ds_read_b128 v[106:109], v200 offset:16192
	s_waitcnt lgkmcnt(6)
	v_pk_mul_f32 v[210:211], v[156:157], v[224:225]
	v_pk_mul_f32 v[212:213], v[126:127], v[156:157]
	v_pk_fma_f32 v[210:211], v[158:159], v[226:227], v[210:211]
	v_pk_fma_f32 v[212:213], v[158:159], v[128:129], v[212:213]
	v_add_f32_e32 v210, v210, v211
	v_add_f32_e32 v212, v212, v213
	v_pk_mul_f32 v[214:215], v[232:233], v[208:209] op_sel_hi:[1,0]
	v_add_f32_dpp v210, v210, v210 quad_perm:[1,0,3,2] row_mask:0xf bank_mask:0xf bound_ctrl:1
	v_add_f32_dpp v212, v212, v212 quad_perm:[1,0,3,2] row_mask:0xf bank_mask:0xf bound_ctrl:1
	v_pk_mul_f32 v[216:217], v[234:235], v[208:209] op_sel_hi:[1,0]
	v_add_f32_dpp v210, v210, v210 quad_perm:[2,3,0,1] row_mask:0xf bank_mask:0xf bound_ctrl:1
	v_add_f32_dpp v212, v212, v212 quad_perm:[2,3,0,1] row_mask:0xf bank_mask:0xf bound_ctrl:1
	ds_read_b128 v[114:117], v200 offset:17488
	v_add_f32_dpp v210, v210, v210 row_half_mirror row_mask:0xf bank_mask:0xf bound_ctrl:1
	v_add_f32_dpp v212, v212, v212 row_half_mirror row_mask:0xf bank_mask:0xf bound_ctrl:1
	ds_read_b128 v[122:125], v200 offset:17520
	v_add_f32_dpp v218, v210, v210 row_mirror row_mask:0xf bank_mask:0xf bound_ctrl:1
	v_add_f32_dpp v240, v212, v212 row_mirror row_mask:0xf bank_mask:0xf bound_ctrl:1
	ds_read_b32 v206, v201 offset:17472
	v_pk_fma_f32 v[214:215], v[218:219], v[228:229], v[214:215] op_sel_hi:[0,1,1]
	v_pk_fma_f32 v[216:217], v[218:219], v[230:231], v[216:217] op_sel_hi:[0,1,1]
	v_cndmask_b32_e64 v241, v241, v240, s[24:25]
	v_pk_fma_f32 v[156:157], v[156:157], v[220:221], v[214:215]
	v_pk_fma_f32 v[158:159], v[158:159], v[222:223], v[216:217]
	ds_read_b128 v[118:121], v200 offset:17504
	ds_read_b128 v[110:113], v200 offset:17472
	ds_read_b128 v[126:129], v200 offset:17536
	s_waitcnt lgkmcnt(6)
	v_pk_mul_f32 v[210:211], v[156:157], v[94:95]
	v_pk_mul_f32 v[212:213], v[236:237], v[156:157]
	v_pk_fma_f32 v[210:211], v[158:159], v[96:97], v[210:211]
	v_pk_fma_f32 v[212:213], v[158:159], v[238:239], v[212:213]
	v_add_f32_e32 v210, v210, v211
	v_add_f32_e32 v212, v212, v213
	v_pk_mul_f32 v[214:215], v[102:103], v[204:205] op_sel_hi:[1,0]
	v_add_f32_dpp v210, v210, v210 quad_perm:[1,0,3,2] row_mask:0xf bank_mask:0xf bound_ctrl:1
	v_add_f32_dpp v212, v212, v212 quad_perm:[1,0,3,2] row_mask:0xf bank_mask:0xf bound_ctrl:1
	v_pk_mul_f32 v[216:217], v[104:105], v[204:205] op_sel_hi:[1,0]
	v_add_f32_dpp v210, v210, v210 quad_perm:[2,3,0,1] row_mask:0xf bank_mask:0xf bound_ctrl:1
	v_add_f32_dpp v212, v212, v212 quad_perm:[2,3,0,1] row_mask:0xf bank_mask:0xf bound_ctrl:1
	ds_read_b128 v[224:227], v200 offset:18832
	v_add_f32_dpp v210, v210, v210 row_half_mirror row_mask:0xf bank_mask:0xf bound_ctrl:1
	v_add_f32_dpp v212, v212, v212 row_half_mirror row_mask:0xf bank_mask:0xf bound_ctrl:1
	ds_read_b128 v[232:235], v200 offset:18864
	v_add_f32_dpp v218, v210, v210 row_mirror row_mask:0xf bank_mask:0xf bound_ctrl:1
	v_add_f32_dpp v240, v212, v212 row_mirror row_mask:0xf bank_mask:0xf bound_ctrl:1
	ds_read_b32 v208, v201 offset:18816
	v_pk_fma_f32 v[214:215], v[218:219], v[98:99], v[214:215] op_sel_hi:[0,1,1]
	v_pk_fma_f32 v[216:217], v[218:219], v[100:101], v[216:217] op_sel_hi:[0,1,1]
	v_cndmask_b32_e64 v241, v241, v240, s[26:27]
	v_pk_fma_f32 v[156:157], v[156:157], v[90:91], v[214:215]
	v_pk_fma_f32 v[158:159], v[158:159], v[92:93], v[216:217]
	ds_read_b128 v[228:231], v200 offset:18848
	ds_read_b128 v[220:223], v200 offset:18816
	ds_read_b128 v[236:239], v200 offset:18880
	s_waitcnt lgkmcnt(6)
	v_pk_mul_f32 v[210:211], v[156:157], v[114:115]
	v_pk_mul_f32 v[212:213], v[106:107], v[156:157]
	v_pk_fma_f32 v[210:211], v[158:159], v[116:117], v[210:211]
	v_pk_fma_f32 v[212:213], v[158:159], v[108:109], v[212:213]
	v_add_f32_e32 v210, v210, v211
	v_add_f32_e32 v212, v212, v213
	v_pk_mul_f32 v[214:215], v[122:123], v[206:207] op_sel_hi:[1,0]
	v_add_f32_dpp v210, v210, v210 quad_perm:[1,0,3,2] row_mask:0xf bank_mask:0xf bound_ctrl:1
	v_add_f32_dpp v212, v212, v212 quad_perm:[1,0,3,2] row_mask:0xf bank_mask:0xf bound_ctrl:1
	v_pk_mul_f32 v[216:217], v[124:125], v[206:207] op_sel_hi:[1,0]
	v_add_f32_dpp v210, v210, v210 quad_perm:[2,3,0,1] row_mask:0xf bank_mask:0xf bound_ctrl:1
	v_add_f32_dpp v212, v212, v212 quad_perm:[2,3,0,1] row_mask:0xf bank_mask:0xf bound_ctrl:1
	ds_read_b128 v[94:97], v200 offset:20176
	v_add_f32_dpp v210, v210, v210 row_half_mirror row_mask:0xf bank_mask:0xf bound_ctrl:1
	v_add_f32_dpp v212, v212, v212 row_half_mirror row_mask:0xf bank_mask:0xf bound_ctrl:1
	ds_read_b128 v[102:105], v200 offset:20208
	v_add_f32_dpp v218, v210, v210 row_mirror row_mask:0xf bank_mask:0xf bound_ctrl:1
	v_add_f32_dpp v240, v212, v212 row_mirror row_mask:0xf bank_mask:0xf bound_ctrl:1
	ds_read_b32 v204, v201 offset:20160
	v_pk_fma_f32 v[214:215], v[218:219], v[118:119], v[214:215] op_sel_hi:[0,1,1]
	v_pk_fma_f32 v[216:217], v[218:219], v[120:121], v[216:217] op_sel_hi:[0,1,1]
	v_cndmask_b32_e64 v241, v241, v240, s[28:29]
	v_pk_fma_f32 v[156:157], v[156:157], v[110:111], v[214:215]
	v_pk_fma_f32 v[158:159], v[158:159], v[112:113], v[216:217]
	ds_read_b128 v[98:101], v200 offset:20192
	ds_read_b128 v[90:93], v200 offset:20160
	ds_read_b128 v[106:109], v200 offset:20224
	s_waitcnt lgkmcnt(6)
	v_pk_mul_f32 v[210:211], v[156:157], v[224:225]
	v_pk_mul_f32 v[212:213], v[126:127], v[156:157]
	v_pk_fma_f32 v[210:211], v[158:159], v[226:227], v[210:211]
	v_pk_fma_f32 v[212:213], v[158:159], v[128:129], v[212:213]
	v_add_f32_e32 v210, v210, v211
	v_add_f32_e32 v212, v212, v213
	v_pk_mul_f32 v[214:215], v[232:233], v[208:209] op_sel_hi:[1,0]
	v_add_f32_dpp v210, v210, v210 quad_perm:[1,0,3,2] row_mask:0xf bank_mask:0xf bound_ctrl:1
	v_add_f32_dpp v212, v212, v212 quad_perm:[1,0,3,2] row_mask:0xf bank_mask:0xf bound_ctrl:1
	v_pk_mul_f32 v[216:217], v[234:235], v[208:209] op_sel_hi:[1,0]
	v_add_f32_dpp v210, v210, v210 quad_perm:[2,3,0,1] row_mask:0xf bank_mask:0xf bound_ctrl:1
	v_add_f32_dpp v212, v212, v212 quad_perm:[2,3,0,1] row_mask:0xf bank_mask:0xf bound_ctrl:1
	ds_read_b128 v[114:117], v200 offset:21520
	v_add_f32_dpp v210, v210, v210 row_half_mirror row_mask:0xf bank_mask:0xf bound_ctrl:1
	v_add_f32_dpp v212, v212, v212 row_half_mirror row_mask:0xf bank_mask:0xf bound_ctrl:1
	ds_read_b128 v[122:125], v200 offset:21552
	v_add_f32_dpp v218, v210, v210 row_mirror row_mask:0xf bank_mask:0xf bound_ctrl:1
	v_add_f32_dpp v240, v212, v212 row_mirror row_mask:0xf bank_mask:0xf bound_ctrl:1
	ds_read_b32 v206, v201 offset:21504
	v_pk_fma_f32 v[214:215], v[218:219], v[228:229], v[214:215] op_sel_hi:[0,1,1]
	v_pk_fma_f32 v[216:217], v[218:219], v[230:231], v[216:217] op_sel_hi:[0,1,1]
	v_cndmask_b32_e64 v241, v241, v240, s[30:31]
	v_pk_fma_f32 v[156:157], v[156:157], v[220:221], v[214:215]
	v_pk_fma_f32 v[158:159], v[158:159], v[222:223], v[216:217]
	ds_read_b128 v[118:121], v200 offset:21536
	ds_read_b128 v[110:113], v200 offset:21504
	ds_read_b128 v[126:129], v200 offset:21568
	s_waitcnt lgkmcnt(6)
	v_pk_mul_f32 v[210:211], v[156:157], v[94:95]
	v_pk_mul_f32 v[212:213], v[236:237], v[156:157]
	v_pk_fma_f32 v[210:211], v[158:159], v[96:97], v[210:211]
	v_pk_fma_f32 v[212:213], v[158:159], v[238:239], v[212:213]
	v_add_f32_e32 v210, v210, v211
	v_add_f32_e32 v212, v212, v213
	v_pk_mul_f32 v[214:215], v[102:103], v[204:205] op_sel_hi:[1,0]
	v_add_f32_dpp v210, v210, v210 quad_perm:[1,0,3,2] row_mask:0xf bank_mask:0xf bound_ctrl:1
	v_add_f32_dpp v212, v212, v212 quad_perm:[1,0,3,2] row_mask:0xf bank_mask:0xf bound_ctrl:1
	v_pk_mul_f32 v[216:217], v[104:105], v[204:205] op_sel_hi:[1,0]
	v_add_f32_dpp v210, v210, v210 quad_perm:[2,3,0,1] row_mask:0xf bank_mask:0xf bound_ctrl:1
	v_add_f32_dpp v212, v212, v212 quad_perm:[2,3,0,1] row_mask:0xf bank_mask:0xf bound_ctrl:1
	ds_read_b128 v[224:227], v200 offset:22864
	v_add_f32_dpp v210, v210, v210 row_half_mirror row_mask:0xf bank_mask:0xf bound_ctrl:1
	v_add_f32_dpp v212, v212, v212 row_half_mirror row_mask:0xf bank_mask:0xf bound_ctrl:1
	ds_read_b128 v[232:235], v200 offset:22896
	v_add_f32_dpp v218, v210, v210 row_mirror row_mask:0xf bank_mask:0xf bound_ctrl:1
	v_add_f32_dpp v240, v212, v212 row_mirror row_mask:0xf bank_mask:0xf bound_ctrl:1
	ds_read_b32 v208, v201 offset:22848
	v_pk_fma_f32 v[214:215], v[218:219], v[98:99], v[214:215] op_sel_hi:[0,1,1]
	v_pk_fma_f32 v[216:217], v[218:219], v[100:101], v[216:217] op_sel_hi:[0,1,1]
	v_cndmask_b32_e64 v241, v241, v240, s[34:35]
	v_pk_fma_f32 v[156:157], v[156:157], v[90:91], v[214:215]
	v_pk_fma_f32 v[158:159], v[158:159], v[92:93], v[216:217]
	ds_read_b128 v[228:231], v200 offset:22880
	ds_read_b128 v[220:223], v200 offset:22848
	ds_read_b128 v[236:239], v200 offset:22912
	s_waitcnt lgkmcnt(6)
	v_pk_mul_f32 v[210:211], v[156:157], v[114:115]
	v_pk_mul_f32 v[212:213], v[106:107], v[156:157]
	v_pk_fma_f32 v[210:211], v[158:159], v[116:117], v[210:211]
	v_pk_fma_f32 v[212:213], v[158:159], v[108:109], v[212:213]
	v_add_f32_e32 v210, v210, v211
	v_add_f32_e32 v212, v212, v213
	v_pk_mul_f32 v[214:215], v[122:123], v[206:207] op_sel_hi:[1,0]
	v_add_f32_dpp v210, v210, v210 quad_perm:[1,0,3,2] row_mask:0xf bank_mask:0xf bound_ctrl:1
	v_add_f32_dpp v212, v212, v212 quad_perm:[1,0,3,2] row_mask:0xf bank_mask:0xf bound_ctrl:1
	v_pk_mul_f32 v[216:217], v[124:125], v[206:207] op_sel_hi:[1,0]
	v_add_f32_dpp v210, v210, v210 quad_perm:[2,3,0,1] row_mask:0xf bank_mask:0xf bound_ctrl:1
	v_add_f32_dpp v212, v212, v212 quad_perm:[2,3,0,1] row_mask:0xf bank_mask:0xf bound_ctrl:1
	ds_read_b128 v[94:97], v200 offset:24208
	v_add_f32_dpp v210, v210, v210 row_half_mirror row_mask:0xf bank_mask:0xf bound_ctrl:1
	v_add_f32_dpp v212, v212, v212 row_half_mirror row_mask:0xf bank_mask:0xf bound_ctrl:1
	ds_read_b128 v[102:105], v200 offset:24240
	v_add_f32_dpp v218, v210, v210 row_mirror row_mask:0xf bank_mask:0xf bound_ctrl:1
	v_add_f32_dpp v240, v212, v212 row_mirror row_mask:0xf bank_mask:0xf bound_ctrl:1
	ds_read_b32 v204, v201 offset:24192
	v_pk_fma_f32 v[214:215], v[218:219], v[118:119], v[214:215] op_sel_hi:[0,1,1]
	v_pk_fma_f32 v[216:217], v[218:219], v[120:121], v[216:217] op_sel_hi:[0,1,1]
	v_cndmask_b32_e64 v241, v241, v240, s[36:37]
	v_pk_fma_f32 v[156:157], v[156:157], v[110:111], v[214:215]
	v_pk_fma_f32 v[158:159], v[158:159], v[112:113], v[216:217]
	ds_read_b128 v[98:101], v200 offset:24224
	ds_read_b128 v[90:93], v200 offset:24192
	ds_read_b128 v[106:109], v200 offset:24256
	s_waitcnt lgkmcnt(6)
	v_pk_mul_f32 v[210:211], v[156:157], v[224:225]
	v_pk_mul_f32 v[212:213], v[126:127], v[156:157]
	v_pk_fma_f32 v[210:211], v[158:159], v[226:227], v[210:211]
	v_pk_fma_f32 v[212:213], v[158:159], v[128:129], v[212:213]
	v_add_f32_e32 v210, v210, v211
	v_add_f32_e32 v212, v212, v213
	v_pk_mul_f32 v[214:215], v[232:233], v[208:209] op_sel_hi:[1,0]
	v_add_f32_dpp v210, v210, v210 quad_perm:[1,0,3,2] row_mask:0xf bank_mask:0xf bound_ctrl:1
	v_add_f32_dpp v212, v212, v212 quad_perm:[1,0,3,2] row_mask:0xf bank_mask:0xf bound_ctrl:1
	v_pk_mul_f32 v[216:217], v[234:235], v[208:209] op_sel_hi:[1,0]
	v_add_f32_dpp v210, v210, v210 quad_perm:[2,3,0,1] row_mask:0xf bank_mask:0xf bound_ctrl:1
	v_add_f32_dpp v212, v212, v212 quad_perm:[2,3,0,1] row_mask:0xf bank_mask:0xf bound_ctrl:1
	ds_read_b128 v[114:117], v200 offset:25552
	v_add_f32_dpp v210, v210, v210 row_half_mirror row_mask:0xf bank_mask:0xf bound_ctrl:1
	v_add_f32_dpp v212, v212, v212 row_half_mirror row_mask:0xf bank_mask:0xf bound_ctrl:1
	ds_read_b128 v[122:125], v200 offset:25584
	v_add_f32_dpp v218, v210, v210 row_mirror row_mask:0xf bank_mask:0xf bound_ctrl:1
	v_add_f32_dpp v240, v212, v212 row_mirror row_mask:0xf bank_mask:0xf bound_ctrl:1
	ds_read_b32 v206, v201 offset:25536
	v_pk_fma_f32 v[214:215], v[218:219], v[228:229], v[214:215] op_sel_hi:[0,1,1]
	v_pk_fma_f32 v[216:217], v[218:219], v[230:231], v[216:217] op_sel_hi:[0,1,1]
	v_cndmask_b32_e64 v242, 0, v240, s[4:5]
	v_pk_fma_f32 v[156:157], v[156:157], v[220:221], v[214:215]
	v_pk_fma_f32 v[158:159], v[158:159], v[222:223], v[216:217]
	ds_read_b128 v[118:121], v200 offset:25568
	ds_read_b128 v[110:113], v200 offset:25536
	ds_read_b128 v[126:129], v200 offset:25600
	s_waitcnt lgkmcnt(6)
	v_pk_mul_f32 v[210:211], v[156:157], v[94:95]
	v_pk_mul_f32 v[212:213], v[236:237], v[156:157]
	v_pk_fma_f32 v[210:211], v[158:159], v[96:97], v[210:211]
	v_pk_fma_f32 v[212:213], v[158:159], v[238:239], v[212:213]
	v_add_f32_e32 v210, v210, v211
	v_add_f32_e32 v212, v212, v213
	v_pk_mul_f32 v[214:215], v[102:103], v[204:205] op_sel_hi:[1,0]
	v_add_f32_dpp v210, v210, v210 quad_perm:[1,0,3,2] row_mask:0xf bank_mask:0xf bound_ctrl:1
	v_add_f32_dpp v212, v212, v212 quad_perm:[1,0,3,2] row_mask:0xf bank_mask:0xf bound_ctrl:1
	v_pk_mul_f32 v[216:217], v[104:105], v[204:205] op_sel_hi:[1,0]
	v_add_f32_dpp v210, v210, v210 quad_perm:[2,3,0,1] row_mask:0xf bank_mask:0xf bound_ctrl:1
	v_add_f32_dpp v212, v212, v212 quad_perm:[2,3,0,1] row_mask:0xf bank_mask:0xf bound_ctrl:1
	ds_read_b128 v[224:227], v200 offset:26896
	v_add_f32_dpp v210, v210, v210 row_half_mirror row_mask:0xf bank_mask:0xf bound_ctrl:1
	v_add_f32_dpp v212, v212, v212 row_half_mirror row_mask:0xf bank_mask:0xf bound_ctrl:1
	ds_read_b128 v[232:235], v200 offset:26928
	v_add_f32_dpp v218, v210, v210 row_mirror row_mask:0xf bank_mask:0xf bound_ctrl:1
	v_add_f32_dpp v240, v212, v212 row_mirror row_mask:0xf bank_mask:0xf bound_ctrl:1
	ds_read_b32 v208, v201 offset:26880
	v_pk_fma_f32 v[214:215], v[218:219], v[98:99], v[214:215] op_sel_hi:[0,1,1]
	v_pk_fma_f32 v[216:217], v[218:219], v[100:101], v[216:217] op_sel_hi:[0,1,1]
	v_cndmask_b32_e64 v242, v242, v240, s[6:7]
	v_pk_fma_f32 v[156:157], v[156:157], v[90:91], v[214:215]
	v_pk_fma_f32 v[158:159], v[158:159], v[92:93], v[216:217]
	ds_read_b128 v[228:231], v200 offset:26912
	ds_read_b128 v[220:223], v200 offset:26880
	ds_read_b128 v[236:239], v200 offset:26944
	s_waitcnt lgkmcnt(6)
	v_pk_mul_f32 v[210:211], v[156:157], v[114:115]
	v_pk_mul_f32 v[212:213], v[106:107], v[156:157]
	v_pk_fma_f32 v[210:211], v[158:159], v[116:117], v[210:211]
	v_pk_fma_f32 v[212:213], v[158:159], v[108:109], v[212:213]
	v_add_f32_e32 v210, v210, v211
	v_add_f32_e32 v212, v212, v213
	v_pk_mul_f32 v[214:215], v[122:123], v[206:207] op_sel_hi:[1,0]
	v_add_f32_dpp v210, v210, v210 quad_perm:[1,0,3,2] row_mask:0xf bank_mask:0xf bound_ctrl:1
	v_add_f32_dpp v212, v212, v212 quad_perm:[1,0,3,2] row_mask:0xf bank_mask:0xf bound_ctrl:1
	v_pk_mul_f32 v[216:217], v[124:125], v[206:207] op_sel_hi:[1,0]
	v_add_f32_dpp v210, v210, v210 quad_perm:[2,3,0,1] row_mask:0xf bank_mask:0xf bound_ctrl:1
	v_add_f32_dpp v212, v212, v212 quad_perm:[2,3,0,1] row_mask:0xf bank_mask:0xf bound_ctrl:1
	ds_read_b128 v[94:97], v200 offset:28240
	v_add_f32_dpp v210, v210, v210 row_half_mirror row_mask:0xf bank_mask:0xf bound_ctrl:1
	v_add_f32_dpp v212, v212, v212 row_half_mirror row_mask:0xf bank_mask:0xf bound_ctrl:1
	ds_read_b128 v[102:105], v200 offset:28272
	v_add_f32_dpp v218, v210, v210 row_mirror row_mask:0xf bank_mask:0xf bound_ctrl:1
	v_add_f32_dpp v240, v212, v212 row_mirror row_mask:0xf bank_mask:0xf bound_ctrl:1
	ds_read_b32 v204, v201 offset:28224
	v_pk_fma_f32 v[214:215], v[218:219], v[118:119], v[214:215] op_sel_hi:[0,1,1]
	v_pk_fma_f32 v[216:217], v[218:219], v[120:121], v[216:217] op_sel_hi:[0,1,1]
	v_cndmask_b32_e64 v242, v242, v240, s[8:9]
	v_pk_fma_f32 v[156:157], v[156:157], v[110:111], v[214:215]
	v_pk_fma_f32 v[158:159], v[158:159], v[112:113], v[216:217]
	ds_read_b128 v[98:101], v200 offset:28256
	ds_read_b128 v[90:93], v200 offset:28224
	ds_read_b128 v[106:109], v200 offset:28288
	s_waitcnt lgkmcnt(6)
	v_pk_mul_f32 v[210:211], v[156:157], v[224:225]
	v_pk_mul_f32 v[212:213], v[126:127], v[156:157]
	v_pk_fma_f32 v[210:211], v[158:159], v[226:227], v[210:211]
	v_pk_fma_f32 v[212:213], v[158:159], v[128:129], v[212:213]
	v_add_f32_e32 v210, v210, v211
	v_add_f32_e32 v212, v212, v213
	v_pk_mul_f32 v[214:215], v[232:233], v[208:209] op_sel_hi:[1,0]
	v_add_f32_dpp v210, v210, v210 quad_perm:[1,0,3,2] row_mask:0xf bank_mask:0xf bound_ctrl:1
	v_add_f32_dpp v212, v212, v212 quad_perm:[1,0,3,2] row_mask:0xf bank_mask:0xf bound_ctrl:1
	v_pk_mul_f32 v[216:217], v[234:235], v[208:209] op_sel_hi:[1,0]
	v_add_f32_dpp v210, v210, v210 quad_perm:[2,3,0,1] row_mask:0xf bank_mask:0xf bound_ctrl:1
	v_add_f32_dpp v212, v212, v212 quad_perm:[2,3,0,1] row_mask:0xf bank_mask:0xf bound_ctrl:1
	ds_read_b128 v[114:117], v200 offset:29584
	v_add_f32_dpp v210, v210, v210 row_half_mirror row_mask:0xf bank_mask:0xf bound_ctrl:1
	v_add_f32_dpp v212, v212, v212 row_half_mirror row_mask:0xf bank_mask:0xf bound_ctrl:1
	ds_read_b128 v[122:125], v200 offset:29616
	v_add_f32_dpp v218, v210, v210 row_mirror row_mask:0xf bank_mask:0xf bound_ctrl:1
	v_add_f32_dpp v240, v212, v212 row_mirror row_mask:0xf bank_mask:0xf bound_ctrl:1
	ds_read_b32 v206, v201 offset:29568
	v_pk_fma_f32 v[214:215], v[218:219], v[228:229], v[214:215] op_sel_hi:[0,1,1]
	v_pk_fma_f32 v[216:217], v[218:219], v[230:231], v[216:217] op_sel_hi:[0,1,1]
	v_cndmask_b32_e64 v242, v242, v240, s[10:11]
	v_pk_fma_f32 v[156:157], v[156:157], v[220:221], v[214:215]
	v_pk_fma_f32 v[158:159], v[158:159], v[222:223], v[216:217]
	ds_read_b128 v[118:121], v200 offset:29600
	ds_read_b128 v[110:113], v200 offset:29568
	ds_read_b128 v[126:129], v200 offset:29632
	s_waitcnt lgkmcnt(6)
	v_pk_mul_f32 v[210:211], v[156:157], v[94:95]
	v_pk_mul_f32 v[212:213], v[236:237], v[156:157]
	v_pk_fma_f32 v[210:211], v[158:159], v[96:97], v[210:211]
	v_pk_fma_f32 v[212:213], v[158:159], v[238:239], v[212:213]
	v_add_f32_e32 v210, v210, v211
	v_add_f32_e32 v212, v212, v213
	v_pk_mul_f32 v[214:215], v[102:103], v[204:205] op_sel_hi:[1,0]
	v_add_f32_dpp v210, v210, v210 quad_perm:[1,0,3,2] row_mask:0xf bank_mask:0xf bound_ctrl:1
	v_add_f32_dpp v212, v212, v212 quad_perm:[1,0,3,2] row_mask:0xf bank_mask:0xf bound_ctrl:1
	v_pk_mul_f32 v[216:217], v[104:105], v[204:205] op_sel_hi:[1,0]
	v_add_f32_dpp v210, v210, v210 quad_perm:[2,3,0,1] row_mask:0xf bank_mask:0xf bound_ctrl:1
	v_add_f32_dpp v212, v212, v212 quad_perm:[2,3,0,1] row_mask:0xf bank_mask:0xf bound_ctrl:1
	ds_read_b128 v[224:227], v200 offset:30928
	v_add_f32_dpp v210, v210, v210 row_half_mirror row_mask:0xf bank_mask:0xf bound_ctrl:1
	v_add_f32_dpp v212, v212, v212 row_half_mirror row_mask:0xf bank_mask:0xf bound_ctrl:1
	ds_read_b128 v[232:235], v200 offset:30960
	v_add_f32_dpp v218, v210, v210 row_mirror row_mask:0xf bank_mask:0xf bound_ctrl:1
	v_add_f32_dpp v240, v212, v212 row_mirror row_mask:0xf bank_mask:0xf bound_ctrl:1
	ds_read_b32 v208, v201 offset:30912
	v_pk_fma_f32 v[214:215], v[218:219], v[98:99], v[214:215] op_sel_hi:[0,1,1]
	v_pk_fma_f32 v[216:217], v[218:219], v[100:101], v[216:217] op_sel_hi:[0,1,1]
	v_cndmask_b32_e64 v242, v242, v240, s[12:13]
	v_pk_fma_f32 v[156:157], v[156:157], v[90:91], v[214:215]
	v_pk_fma_f32 v[158:159], v[158:159], v[92:93], v[216:217]
	ds_read_b128 v[228:231], v200 offset:30944
	ds_read_b128 v[220:223], v200 offset:30912
	ds_read_b128 v[236:239], v200 offset:30976
	s_waitcnt lgkmcnt(6)
	v_pk_mul_f32 v[210:211], v[156:157], v[114:115]
	v_pk_mul_f32 v[212:213], v[106:107], v[156:157]
	v_pk_fma_f32 v[210:211], v[158:159], v[116:117], v[210:211]
	v_pk_fma_f32 v[212:213], v[158:159], v[108:109], v[212:213]
	v_add_f32_e32 v210, v210, v211
	v_add_f32_e32 v212, v212, v213
	v_pk_mul_f32 v[214:215], v[122:123], v[206:207] op_sel_hi:[1,0]
	v_add_f32_dpp v210, v210, v210 quad_perm:[1,0,3,2] row_mask:0xf bank_mask:0xf bound_ctrl:1
	v_add_f32_dpp v212, v212, v212 quad_perm:[1,0,3,2] row_mask:0xf bank_mask:0xf bound_ctrl:1
	v_pk_mul_f32 v[216:217], v[124:125], v[206:207] op_sel_hi:[1,0]
	v_add_f32_dpp v210, v210, v210 quad_perm:[2,3,0,1] row_mask:0xf bank_mask:0xf bound_ctrl:1
	v_add_f32_dpp v212, v212, v212 quad_perm:[2,3,0,1] row_mask:0xf bank_mask:0xf bound_ctrl:1
	ds_read_b128 v[94:97], v200 offset:32272
	v_add_f32_dpp v210, v210, v210 row_half_mirror row_mask:0xf bank_mask:0xf bound_ctrl:1
	v_add_f32_dpp v212, v212, v212 row_half_mirror row_mask:0xf bank_mask:0xf bound_ctrl:1
	ds_read_b128 v[102:105], v200 offset:32304
	v_add_f32_dpp v218, v210, v210 row_mirror row_mask:0xf bank_mask:0xf bound_ctrl:1
	v_add_f32_dpp v240, v212, v212 row_mirror row_mask:0xf bank_mask:0xf bound_ctrl:1
	ds_read_b32 v204, v201 offset:32256
	v_pk_fma_f32 v[214:215], v[218:219], v[118:119], v[214:215] op_sel_hi:[0,1,1]
	v_pk_fma_f32 v[216:217], v[218:219], v[120:121], v[216:217] op_sel_hi:[0,1,1]
	v_cndmask_b32_e64 v242, v242, v240, s[14:15]
	v_pk_fma_f32 v[156:157], v[156:157], v[110:111], v[214:215]
	v_pk_fma_f32 v[158:159], v[158:159], v[112:113], v[216:217]
	ds_read_b128 v[98:101], v200 offset:32288
	ds_read_b128 v[90:93], v200 offset:32256
	ds_read_b128 v[106:109], v200 offset:32320
	s_waitcnt lgkmcnt(6)
	v_pk_mul_f32 v[210:211], v[156:157], v[224:225]
	v_pk_mul_f32 v[212:213], v[126:127], v[156:157]
	v_pk_fma_f32 v[210:211], v[158:159], v[226:227], v[210:211]
	v_pk_fma_f32 v[212:213], v[158:159], v[128:129], v[212:213]
	v_add_f32_e32 v210, v210, v211
	v_add_f32_e32 v212, v212, v213
	v_pk_mul_f32 v[214:215], v[232:233], v[208:209] op_sel_hi:[1,0]
	v_add_f32_dpp v210, v210, v210 quad_perm:[1,0,3,2] row_mask:0xf bank_mask:0xf bound_ctrl:1
	v_add_f32_dpp v212, v212, v212 quad_perm:[1,0,3,2] row_mask:0xf bank_mask:0xf bound_ctrl:1
	v_pk_mul_f32 v[216:217], v[234:235], v[208:209] op_sel_hi:[1,0]
	v_add_f32_dpp v210, v210, v210 quad_perm:[2,3,0,1] row_mask:0xf bank_mask:0xf bound_ctrl:1
	v_add_f32_dpp v212, v212, v212 quad_perm:[2,3,0,1] row_mask:0xf bank_mask:0xf bound_ctrl:1
	ds_read_b128 v[114:117], v200 offset:33616
	v_add_f32_dpp v210, v210, v210 row_half_mirror row_mask:0xf bank_mask:0xf bound_ctrl:1
	v_add_f32_dpp v212, v212, v212 row_half_mirror row_mask:0xf bank_mask:0xf bound_ctrl:1
	ds_read_b128 v[122:125], v200 offset:33648
	v_add_f32_dpp v218, v210, v210 row_mirror row_mask:0xf bank_mask:0xf bound_ctrl:1
	v_add_f32_dpp v240, v212, v212 row_mirror row_mask:0xf bank_mask:0xf bound_ctrl:1
	ds_read_b32 v206, v201 offset:33600
	v_pk_fma_f32 v[214:215], v[218:219], v[228:229], v[214:215] op_sel_hi:[0,1,1]
	v_pk_fma_f32 v[216:217], v[218:219], v[230:231], v[216:217] op_sel_hi:[0,1,1]
	v_cndmask_b32_e64 v242, v242, v240, s[16:17]
	v_pk_fma_f32 v[156:157], v[156:157], v[220:221], v[214:215]
	v_pk_fma_f32 v[158:159], v[158:159], v[222:223], v[216:217]
	ds_read_b128 v[118:121], v200 offset:33632
	ds_read_b128 v[110:113], v200 offset:33600
	ds_read_b128 v[126:129], v200 offset:33664
	s_waitcnt lgkmcnt(6)
	v_pk_mul_f32 v[210:211], v[156:157], v[94:95]
	v_pk_mul_f32 v[212:213], v[236:237], v[156:157]
	v_pk_fma_f32 v[210:211], v[158:159], v[96:97], v[210:211]
	v_pk_fma_f32 v[212:213], v[158:159], v[238:239], v[212:213]
	v_add_f32_e32 v210, v210, v211
	v_add_f32_e32 v212, v212, v213
	v_pk_mul_f32 v[214:215], v[102:103], v[204:205] op_sel_hi:[1,0]
	v_add_f32_dpp v210, v210, v210 quad_perm:[1,0,3,2] row_mask:0xf bank_mask:0xf bound_ctrl:1
	v_add_f32_dpp v212, v212, v212 quad_perm:[1,0,3,2] row_mask:0xf bank_mask:0xf bound_ctrl:1
	v_pk_mul_f32 v[216:217], v[104:105], v[204:205] op_sel_hi:[1,0]
	v_add_f32_dpp v210, v210, v210 quad_perm:[2,3,0,1] row_mask:0xf bank_mask:0xf bound_ctrl:1
	v_add_f32_dpp v212, v212, v212 quad_perm:[2,3,0,1] row_mask:0xf bank_mask:0xf bound_ctrl:1
	ds_read_b128 v[224:227], v200 offset:34960
	v_add_f32_dpp v210, v210, v210 row_half_mirror row_mask:0xf bank_mask:0xf bound_ctrl:1
	v_add_f32_dpp v212, v212, v212 row_half_mirror row_mask:0xf bank_mask:0xf bound_ctrl:1
	ds_read_b128 v[232:235], v200 offset:34992
	v_add_f32_dpp v218, v210, v210 row_mirror row_mask:0xf bank_mask:0xf bound_ctrl:1
	v_add_f32_dpp v240, v212, v212 row_mirror row_mask:0xf bank_mask:0xf bound_ctrl:1
	ds_read_b32 v208, v201 offset:34944
	v_pk_fma_f32 v[214:215], v[218:219], v[98:99], v[214:215] op_sel_hi:[0,1,1]
	v_pk_fma_f32 v[216:217], v[218:219], v[100:101], v[216:217] op_sel_hi:[0,1,1]
	v_cndmask_b32_e64 v242, v242, v240, s[18:19]
	v_pk_fma_f32 v[156:157], v[156:157], v[90:91], v[214:215]
	v_pk_fma_f32 v[158:159], v[158:159], v[92:93], v[216:217]
	ds_read_b128 v[228:231], v200 offset:34976
	ds_read_b128 v[220:223], v200 offset:34944
	ds_read_b128 v[236:239], v200 offset:35008
	s_waitcnt lgkmcnt(6)
	v_pk_mul_f32 v[210:211], v[156:157], v[114:115]
	v_pk_mul_f32 v[212:213], v[106:107], v[156:157]
	v_pk_fma_f32 v[210:211], v[158:159], v[116:117], v[210:211]
	v_pk_fma_f32 v[212:213], v[158:159], v[108:109], v[212:213]
	v_add_f32_e32 v210, v210, v211
	v_add_f32_e32 v212, v212, v213
	v_pk_mul_f32 v[214:215], v[122:123], v[206:207] op_sel_hi:[1,0]
	v_add_f32_dpp v210, v210, v210 quad_perm:[1,0,3,2] row_mask:0xf bank_mask:0xf bound_ctrl:1
	v_add_f32_dpp v212, v212, v212 quad_perm:[1,0,3,2] row_mask:0xf bank_mask:0xf bound_ctrl:1
	v_pk_mul_f32 v[216:217], v[124:125], v[206:207] op_sel_hi:[1,0]
	v_add_f32_dpp v210, v210, v210 quad_perm:[2,3,0,1] row_mask:0xf bank_mask:0xf bound_ctrl:1
	v_add_f32_dpp v212, v212, v212 quad_perm:[2,3,0,1] row_mask:0xf bank_mask:0xf bound_ctrl:1
	ds_read_b128 v[94:97], v200 offset:36304
	v_add_f32_dpp v210, v210, v210 row_half_mirror row_mask:0xf bank_mask:0xf bound_ctrl:1
	v_add_f32_dpp v212, v212, v212 row_half_mirror row_mask:0xf bank_mask:0xf bound_ctrl:1
	ds_read_b128 v[102:105], v200 offset:36336
	v_add_f32_dpp v218, v210, v210 row_mirror row_mask:0xf bank_mask:0xf bound_ctrl:1
	v_add_f32_dpp v240, v212, v212 row_mirror row_mask:0xf bank_mask:0xf bound_ctrl:1
	ds_read_b32 v204, v201 offset:36288
	v_pk_fma_f32 v[214:215], v[218:219], v[118:119], v[214:215] op_sel_hi:[0,1,1]
	v_pk_fma_f32 v[216:217], v[218:219], v[120:121], v[216:217] op_sel_hi:[0,1,1]
	v_cndmask_b32_e64 v242, v242, v240, s[20:21]
	v_pk_fma_f32 v[156:157], v[156:157], v[110:111], v[214:215]
	v_pk_fma_f32 v[158:159], v[158:159], v[112:113], v[216:217]
	ds_read_b128 v[98:101], v200 offset:36320
	ds_read_b128 v[90:93], v200 offset:36288
	ds_read_b128 v[106:109], v200 offset:36352
	s_waitcnt lgkmcnt(6)
	v_pk_mul_f32 v[210:211], v[156:157], v[224:225]
	v_pk_mul_f32 v[212:213], v[126:127], v[156:157]
	v_pk_fma_f32 v[210:211], v[158:159], v[226:227], v[210:211]
	v_pk_fma_f32 v[212:213], v[158:159], v[128:129], v[212:213]
	v_add_f32_e32 v210, v210, v211
	v_add_f32_e32 v212, v212, v213
	v_pk_mul_f32 v[214:215], v[232:233], v[208:209] op_sel_hi:[1,0]
	v_add_f32_dpp v210, v210, v210 quad_perm:[1,0,3,2] row_mask:0xf bank_mask:0xf bound_ctrl:1
	v_add_f32_dpp v212, v212, v212 quad_perm:[1,0,3,2] row_mask:0xf bank_mask:0xf bound_ctrl:1
	v_pk_mul_f32 v[216:217], v[234:235], v[208:209] op_sel_hi:[1,0]
	v_add_f32_dpp v210, v210, v210 quad_perm:[2,3,0,1] row_mask:0xf bank_mask:0xf bound_ctrl:1
	v_add_f32_dpp v212, v212, v212 quad_perm:[2,3,0,1] row_mask:0xf bank_mask:0xf bound_ctrl:1
	ds_read_b128 v[114:117], v200 offset:37648
	v_add_f32_dpp v210, v210, v210 row_half_mirror row_mask:0xf bank_mask:0xf bound_ctrl:1
	v_add_f32_dpp v212, v212, v212 row_half_mirror row_mask:0xf bank_mask:0xf bound_ctrl:1
	ds_read_b128 v[122:125], v200 offset:37680
	v_add_f32_dpp v218, v210, v210 row_mirror row_mask:0xf bank_mask:0xf bound_ctrl:1
	v_add_f32_dpp v240, v212, v212 row_mirror row_mask:0xf bank_mask:0xf bound_ctrl:1
	ds_read_b32 v206, v201 offset:37632
	v_pk_fma_f32 v[214:215], v[218:219], v[228:229], v[214:215] op_sel_hi:[0,1,1]
	v_pk_fma_f32 v[216:217], v[218:219], v[230:231], v[216:217] op_sel_hi:[0,1,1]
	v_cndmask_b32_e64 v242, v242, v240, s[22:23]
	v_pk_fma_f32 v[156:157], v[156:157], v[220:221], v[214:215]
	v_pk_fma_f32 v[158:159], v[158:159], v[222:223], v[216:217]
	ds_read_b128 v[118:121], v200 offset:37664
	ds_read_b128 v[110:113], v200 offset:37632
	ds_read_b128 v[126:129], v200 offset:37696
	s_waitcnt lgkmcnt(6)
	v_pk_mul_f32 v[210:211], v[156:157], v[94:95]
	v_pk_mul_f32 v[212:213], v[236:237], v[156:157]
	v_pk_fma_f32 v[210:211], v[158:159], v[96:97], v[210:211]
	v_pk_fma_f32 v[212:213], v[158:159], v[238:239], v[212:213]
	v_add_f32_e32 v210, v210, v211
	v_add_f32_e32 v212, v212, v213
	v_pk_mul_f32 v[214:215], v[102:103], v[204:205] op_sel_hi:[1,0]
	v_add_f32_dpp v210, v210, v210 quad_perm:[1,0,3,2] row_mask:0xf bank_mask:0xf bound_ctrl:1
	v_add_f32_dpp v212, v212, v212 quad_perm:[1,0,3,2] row_mask:0xf bank_mask:0xf bound_ctrl:1
	v_pk_mul_f32 v[216:217], v[104:105], v[204:205] op_sel_hi:[1,0]
	v_add_f32_dpp v210, v210, v210 quad_perm:[2,3,0,1] row_mask:0xf bank_mask:0xf bound_ctrl:1
	v_add_f32_dpp v212, v212, v212 quad_perm:[2,3,0,1] row_mask:0xf bank_mask:0xf bound_ctrl:1
	ds_read_b128 v[224:227], v200 offset:38992
	v_add_f32_dpp v210, v210, v210 row_half_mirror row_mask:0xf bank_mask:0xf bound_ctrl:1
	v_add_f32_dpp v212, v212, v212 row_half_mirror row_mask:0xf bank_mask:0xf bound_ctrl:1
	ds_read_b128 v[232:235], v200 offset:39024
	v_add_f32_dpp v218, v210, v210 row_mirror row_mask:0xf bank_mask:0xf bound_ctrl:1
	v_add_f32_dpp v240, v212, v212 row_mirror row_mask:0xf bank_mask:0xf bound_ctrl:1
	ds_read_b32 v208, v201 offset:38976
	v_pk_fma_f32 v[214:215], v[218:219], v[98:99], v[214:215] op_sel_hi:[0,1,1]
	v_pk_fma_f32 v[216:217], v[218:219], v[100:101], v[216:217] op_sel_hi:[0,1,1]
	v_cndmask_b32_e64 v242, v242, v240, s[24:25]
	v_pk_fma_f32 v[156:157], v[156:157], v[90:91], v[214:215]
	v_pk_fma_f32 v[158:159], v[158:159], v[92:93], v[216:217]
	ds_read_b128 v[228:231], v200 offset:39008
	ds_read_b128 v[220:223], v200 offset:38976
	ds_read_b128 v[236:239], v200 offset:39040
	s_waitcnt lgkmcnt(6)
	v_pk_mul_f32 v[210:211], v[156:157], v[114:115]
	v_pk_mul_f32 v[212:213], v[106:107], v[156:157]
	v_pk_fma_f32 v[210:211], v[158:159], v[116:117], v[210:211]
	v_pk_fma_f32 v[212:213], v[158:159], v[108:109], v[212:213]
	v_add_f32_e32 v210, v210, v211
	v_add_f32_e32 v212, v212, v213
	v_pk_mul_f32 v[214:215], v[122:123], v[206:207] op_sel_hi:[1,0]
	v_add_f32_dpp v210, v210, v210 quad_perm:[1,0,3,2] row_mask:0xf bank_mask:0xf bound_ctrl:1
	v_add_f32_dpp v212, v212, v212 quad_perm:[1,0,3,2] row_mask:0xf bank_mask:0xf bound_ctrl:1
	v_pk_mul_f32 v[216:217], v[124:125], v[206:207] op_sel_hi:[1,0]
	v_add_f32_dpp v210, v210, v210 quad_perm:[2,3,0,1] row_mask:0xf bank_mask:0xf bound_ctrl:1
	v_add_f32_dpp v212, v212, v212 quad_perm:[2,3,0,1] row_mask:0xf bank_mask:0xf bound_ctrl:1
	ds_read_b128 v[94:97], v200 offset:40336
	v_add_f32_dpp v210, v210, v210 row_half_mirror row_mask:0xf bank_mask:0xf bound_ctrl:1
	v_add_f32_dpp v212, v212, v212 row_half_mirror row_mask:0xf bank_mask:0xf bound_ctrl:1
	ds_read_b128 v[102:105], v200 offset:40368
	v_add_f32_dpp v218, v210, v210 row_mirror row_mask:0xf bank_mask:0xf bound_ctrl:1
	v_add_f32_dpp v240, v212, v212 row_mirror row_mask:0xf bank_mask:0xf bound_ctrl:1
	ds_read_b32 v204, v201 offset:40320
	v_pk_fma_f32 v[214:215], v[218:219], v[118:119], v[214:215] op_sel_hi:[0,1,1]
	v_pk_fma_f32 v[216:217], v[218:219], v[120:121], v[216:217] op_sel_hi:[0,1,1]
	v_cndmask_b32_e64 v242, v242, v240, s[26:27]
	v_pk_fma_f32 v[156:157], v[156:157], v[110:111], v[214:215]
	v_pk_fma_f32 v[158:159], v[158:159], v[112:113], v[216:217]
	ds_read_b128 v[98:101], v200 offset:40352
	ds_read_b128 v[90:93], v200 offset:40320
	ds_read_b128 v[106:109], v200 offset:40384
	s_waitcnt lgkmcnt(6)
	v_pk_mul_f32 v[210:211], v[156:157], v[224:225]
	v_pk_mul_f32 v[212:213], v[126:127], v[156:157]
	v_pk_fma_f32 v[210:211], v[158:159], v[226:227], v[210:211]
	v_pk_fma_f32 v[212:213], v[158:159], v[128:129], v[212:213]
	v_add_f32_e32 v210, v210, v211
	v_add_f32_e32 v212, v212, v213
	v_pk_mul_f32 v[214:215], v[232:233], v[208:209] op_sel_hi:[1,0]
	v_add_f32_dpp v210, v210, v210 quad_perm:[1,0,3,2] row_mask:0xf bank_mask:0xf bound_ctrl:1
	v_add_f32_dpp v212, v212, v212 quad_perm:[1,0,3,2] row_mask:0xf bank_mask:0xf bound_ctrl:1
	v_pk_mul_f32 v[216:217], v[234:235], v[208:209] op_sel_hi:[1,0]
	v_add_f32_dpp v210, v210, v210 quad_perm:[2,3,0,1] row_mask:0xf bank_mask:0xf bound_ctrl:1
	v_add_f32_dpp v212, v212, v212 quad_perm:[2,3,0,1] row_mask:0xf bank_mask:0xf bound_ctrl:1
	ds_read_b128 v[114:117], v200 offset:41680
	v_add_f32_dpp v210, v210, v210 row_half_mirror row_mask:0xf bank_mask:0xf bound_ctrl:1
	v_add_f32_dpp v212, v212, v212 row_half_mirror row_mask:0xf bank_mask:0xf bound_ctrl:1
	ds_read_b128 v[122:125], v200 offset:41712
	v_add_f32_dpp v218, v210, v210 row_mirror row_mask:0xf bank_mask:0xf bound_ctrl:1
	v_add_f32_dpp v240, v212, v212 row_mirror row_mask:0xf bank_mask:0xf bound_ctrl:1
	ds_read_b32 v206, v201 offset:41664
	v_pk_fma_f32 v[214:215], v[218:219], v[228:229], v[214:215] op_sel_hi:[0,1,1]
	v_pk_fma_f32 v[216:217], v[218:219], v[230:231], v[216:217] op_sel_hi:[0,1,1]
	v_cndmask_b32_e64 v242, v242, v240, s[28:29]
	v_pk_fma_f32 v[156:157], v[156:157], v[220:221], v[214:215]
	v_pk_fma_f32 v[158:159], v[158:159], v[222:223], v[216:217]
	ds_read_b128 v[118:121], v200 offset:41696
	ds_read_b128 v[110:113], v200 offset:41664
	ds_read_b128 v[126:129], v200 offset:41728
	s_waitcnt lgkmcnt(6)
	v_pk_mul_f32 v[210:211], v[156:157], v[94:95]
	v_pk_mul_f32 v[212:213], v[236:237], v[156:157]
	v_pk_fma_f32 v[210:211], v[158:159], v[96:97], v[210:211]
	v_pk_fma_f32 v[212:213], v[158:159], v[238:239], v[212:213]
	v_add_f32_e32 v210, v210, v211
	v_add_f32_e32 v212, v212, v213
	v_pk_mul_f32 v[214:215], v[102:103], v[204:205] op_sel_hi:[1,0]
	v_add_f32_dpp v210, v210, v210 quad_perm:[1,0,3,2] row_mask:0xf bank_mask:0xf bound_ctrl:1
	v_add_f32_dpp v212, v212, v212 quad_perm:[1,0,3,2] row_mask:0xf bank_mask:0xf bound_ctrl:1
	v_pk_mul_f32 v[216:217], v[104:105], v[204:205] op_sel_hi:[1,0]
	v_add_f32_dpp v210, v210, v210 quad_perm:[2,3,0,1] row_mask:0xf bank_mask:0xf bound_ctrl:1
	v_add_f32_dpp v212, v212, v212 quad_perm:[2,3,0,1] row_mask:0xf bank_mask:0xf bound_ctrl:1
	s_nop 0
	v_add_f32_dpp v210, v210, v210 row_half_mirror row_mask:0xf bank_mask:0xf bound_ctrl:1
	v_add_f32_dpp v212, v212, v212 row_half_mirror row_mask:0xf bank_mask:0xf bound_ctrl:1
	s_nop 0
	v_add_f32_dpp v218, v210, v210 row_mirror row_mask:0xf bank_mask:0xf bound_ctrl:1
	v_add_f32_dpp v240, v212, v212 row_mirror row_mask:0xf bank_mask:0xf bound_ctrl:1
	s_nop 0
	v_pk_fma_f32 v[214:215], v[218:219], v[98:99], v[214:215] op_sel_hi:[0,1,1]
	v_pk_fma_f32 v[216:217], v[218:219], v[100:101], v[216:217] op_sel_hi:[0,1,1]
	v_cndmask_b32_e64 v242, v242, v240, s[30:31]
	v_pk_fma_f32 v[156:157], v[156:157], v[90:91], v[214:215]
	v_pk_fma_f32 v[158:159], v[158:159], v[92:93], v[216:217]
	s_nop 0
	s_nop 0
	s_nop 0
	s_waitcnt lgkmcnt(0)
	v_pk_mul_f32 v[210:211], v[156:157], v[114:115]
	v_pk_mul_f32 v[212:213], v[106:107], v[156:157]
	v_pk_fma_f32 v[210:211], v[158:159], v[116:117], v[210:211]
	v_pk_fma_f32 v[212:213], v[158:159], v[108:109], v[212:213]
	v_add_f32_e32 v210, v210, v211
	v_add_f32_e32 v212, v212, v213
	v_pk_mul_f32 v[214:215], v[122:123], v[206:207] op_sel_hi:[1,0]
	v_add_f32_dpp v210, v210, v210 quad_perm:[1,0,3,2] row_mask:0xf bank_mask:0xf bound_ctrl:1
	v_add_f32_dpp v212, v212, v212 quad_perm:[1,0,3,2] row_mask:0xf bank_mask:0xf bound_ctrl:1
	v_pk_mul_f32 v[216:217], v[124:125], v[206:207] op_sel_hi:[1,0]
	v_add_f32_dpp v210, v210, v210 quad_perm:[2,3,0,1] row_mask:0xf bank_mask:0xf bound_ctrl:1
	v_add_f32_dpp v212, v212, v212 quad_perm:[2,3,0,1] row_mask:0xf bank_mask:0xf bound_ctrl:1
	s_nop 0
	v_add_f32_dpp v210, v210, v210 row_half_mirror row_mask:0xf bank_mask:0xf bound_ctrl:1
	v_add_f32_dpp v212, v212, v212 row_half_mirror row_mask:0xf bank_mask:0xf bound_ctrl:1
	s_nop 0
	v_add_f32_dpp v218, v210, v210 row_mirror row_mask:0xf bank_mask:0xf bound_ctrl:1
	v_add_f32_dpp v240, v212, v212 row_mirror row_mask:0xf bank_mask:0xf bound_ctrl:1
	s_nop 0
	v_pk_fma_f32 v[214:215], v[218:219], v[118:119], v[214:215] op_sel_hi:[0,1,1]
	v_pk_fma_f32 v[216:217], v[218:219], v[120:121], v[216:217] op_sel_hi:[0,1,1]
	v_cndmask_b32_e64 v242, v242, v240, s[34:35]
	v_pk_fma_f32 v[156:157], v[156:157], v[110:111], v[214:215]
	v_pk_fma_f32 v[158:159], v[158:159], v[112:113], v[216:217]
	s_nop 0
	s_nop 0
	s_nop 0
	s_nop 0
	v_pk_mul_f32 v[212:213], v[126:127], v[156:157]
	s_nop 0
	v_pk_fma_f32 v[212:213], v[158:159], v[128:129], v[212:213]
	s_nop 0
	v_add_f32_e32 v212, v212, v213
	s_nop 0
	s_nop 0
	v_add_f32_dpp v212, v212, v212 quad_perm:[1,0,3,2] row_mask:0xf bank_mask:0xf bound_ctrl:1
	s_nop 0
	s_nop 0
	v_add_f32_dpp v212, v212, v212 quad_perm:[2,3,0,1] row_mask:0xf bank_mask:0xf bound_ctrl:1
	s_nop 0
	s_nop 0
	v_add_f32_dpp v212, v212, v212 row_half_mirror row_mask:0xf bank_mask:0xf bound_ctrl:1
	s_nop 0
	s_nop 0
	v_add_f32_dpp v240, v212, v212 row_mirror row_mask:0xf bank_mask:0xf bound_ctrl:1
	s_nop 0
	s_nop 0
	s_nop 0
	v_cndmask_b32_e64 v242, v242, v240, s[36:37]
	v_or_b32_e32 v100, s56, v137
	v_xad_u32 v101, v100, -1, s58
	v_or_b32_e32 v103, 16, v100
	v_cndmask_b32_e64 v100, v101, v100, s[38:39]
	v_bitop3_b32 v102, s56, v202, v137 bitop3:0x36
	v_add_u32_e32 v102, s58, v102
	v_cndmask_b32_e64 v102, v102, v103, s[38:39]
	v_add_u32_e32 v100, s57, v100
	v_add_u32_e32 v102, s57, v102
	v_ashrrev_i32_e32 v101, 31, v100
	v_ashrrev_i32_e32 v103, 31, v102
	v_lshlrev_b64 v[100:101], 12, v[100:101]
	v_lshlrev_b64 v[102:103], 12, v[102:103]
	v_lshl_add_u64 v[100:101], v[148:149], 0, v[100:101]
	v_lshl_add_u64 v[102:103], v[148:149], 0, v[102:103]
	global_store_dword v[100:101], v241, off
	global_store_dword v[102:103], v242, off
	v_mov_b64_e32 v[94:95], v[156:157]
	v_mov_b64_e32 v[96:97], v[158:159]
	s_setprio 0
	s_add_i32 s58, s33, s88
	s_mov_b64 s[56:57], 0
